# v22 + nt on P4's read-once gate-logit loads
# baseline (speedup 1.0000x reference)
; #define LAS __attribute__((address_space(3)))
; __device__ __forceinline__ unsigned pk4_fp8(float a, float b, float c, float d) { int w = 0; w = __builtin_amdgcn_cvt_pk_fp8_f32(a, b, w, false); w = __builtin_amdgcn_cvt_pk_fp8_f32(c, d, w, true); return (unsigned)w; }
; __device__ __forceinline__ float bf_lo(unsigned w) { return __uint_as_float(w << 16); }
; __device__ __forceinline__ float bf_hi(unsigned w) { return __uint_as_float(w & 0xffff0000u); }
; __device__ __forceinline__ float sigmoidf_fast(float x) { return __builtin_amdgcn_rcpf(1.0f + __builtin_amdgcn_exp2f(-1.4426950408889634f * x)); }
;     __device__ __forceinline__ void operator()(f32x4 (&acc)[2][2][4][2], const Unit& u, int wr, int wc, int fr, int fq) const {
;     ...
;                 const size_t ro = (size_t)(u.row0 + ai * 128 + wr * 64 + m * 16 + fr) * DM + col0;
; #pragma unroll
;                 for (int bj = 0; bj < 2; ++bj) {
;                     const u32x4 gd = *(const u32x4*)(GDF + ro + bj * 32);
;                     const float ed[8] = {bf_lo(gd.x), bf_hi(gd.x), bf_lo(gd.y), bf_hi(gd.y), bf_lo(gd.z), bf_hi(gd.z), bf_lo(gd.w), bf_hi(gd.w)};
;                     if (u.tag == 0) {
;                         const u32x4 gn = *(const u32x4*)(GNA + ro + bj * 32);
;                         const float en[8] = {bf_lo(gn.x), bf_hi(gn.x), bf_lo(gn.y), bf_hi(gn.y), bf_lo(gn.z), bf_hi(gn.z), bf_lo(gn.w), bf_hi(gn.w)};
; #pragma unroll
;                         for (int e = 0; e < 8; ++e) {
;                             const float r = (1.0f + __builtin_amdgcn_exp2f(-1.4426950408889634f * ed[e])) * __builtin_amdgcn_rcpf(1.0f + __builtin_amdgcn_exp2f(-1.4426950408889634f * en[e]));
;                             acc[ai][bj][m][e >> 2][e & 3] *= r; }
;                     } else {
;                         float y[8];
; #pragma unroll
;                         for (int e = 0; e < 8; ++e) y[e] = acc[ai][bj][m][e >> 2][e & 3] * sigmoidf_fast(ed[e]) * (PSCALE * WSCALE_INV * OSCALE_INV);
;                         u32x2 w; w.x = pk4_fp8(y[0], y[1], y[2], y[3]); w.y = pk4_fp8(y[4], y[5], y[6], y[7]);
;                         *(LAS u32x2*)(my + fr * 80 + bj * 32 + fq * 8) = w;
;                     }
.LBB0_561:
	s_nop 15
	s_nop 15
	v_add_u32_e32 v4, s76, v164
	v_add_u32_e32 v2, s54, v167
	v_ashrrev_i32_e32 v5, 31, v4
	v_ashrrev_i32_e32 v3, 31, v2
	v_lshlrev_b64 v[6:7], 11, v[4:5]
	v_lshl_add_u64 v[8:9], v[6:7], 0, v[2:3]
	v_lshl_add_u64 v[6:7], v[8:9], 1, s[40:41]
	global_load_dwordx4 v[156:159], v[6:7], off nt
	v_cndmask_b32_e64 v5, 0, 1, s[58:59]
	v_cmp_ne_u32_e64 s[4:5], 1, v5
	s_andn2_b64 vcc, exec, s[58:59]
	s_mov_b64 s[58:59], -1
	s_waitcnt vmcnt(0)
	v_lshlrev_b32_e32 v160, 16, v156
	v_and_b32_e32 v156, 0xffff0000, v156
	v_lshlrev_b32_e32 v161, 16, v157
	v_and_b32_e32 v157, 0xffff0000, v157
	v_lshlrev_b32_e32 v162, 16, v158
	v_and_b32_e32 v158, 0xffff0000, v158
	v_lshlrev_b32_e32 v163, 16, v159
	v_and_b32_e32 v159, 0xffff0000, v159
	v_mul_f32_e32 v160, 0xbfb8aa3b, v160
	v_mul_f32_e32 v156, 0xbfb8aa3b, v156
	v_mul_f32_e32 v181, 0xbfb8aa3b, v161
	v_mul_f32_e32 v157, 0xbfb8aa3b, v157
	v_mul_f32_e32 v182, 0xbfb8aa3b, v162
	v_mul_f32_e32 v158, 0xbfb8aa3b, v158
	v_mul_f32_e32 v183, 0xbfb8aa3b, v163
	v_mul_f32_e32 v159, 0xbfb8aa3b, v159
	v_exp_f32_e32 v160, v160
	v_exp_f32_e32 v161, v156
	v_exp_f32_e32 v162, v181
	v_exp_f32_e32 v163, v157
	v_exp_f32_e32 v156, v182
	v_exp_f32_e32 v157, v158
	v_exp_f32_e32 v158, v183
	v_exp_f32_e32 v159, v159
	s_cbranch_vccnz .LBB0_563
	v_add_f32_e32 v182, 1.0, v162
	v_rcp_f32_e32 v182, v182
	v_add_f32_e32 v183, 1.0, v163
	v_rcp_f32_e32 v183, v183
	v_add_f32_e32 v184, 1.0, v156
	v_rcp_f32_e32 v184, v184
	v_mul_f32_e32 v182, v136, v182
	v_mul_f32_e32 v185, 0x3c000000, v182
	v_mul_f32_e32 v182, v137, v183
	v_add_f32_e32 v183, 1.0, v157
	v_mul_f32_e32 v186, 0x3c000000, v182
	v_mul_f32_e32 v182, v130, v184
	v_rcp_f32_e32 v183, v183
	v_add_f32_e32 v184, 1.0, v158
	v_rcp_f32_e32 v184, v184
	v_add_f32_e32 v5, 1.0, v160
	v_add_f32_e32 v181, 1.0, v161
	v_rcp_f32_e32 v5, v5
	v_rcp_f32_e32 v181, v181
	v_mul_f32_e32 v187, 0x3c000000, v182
	v_mul_f32_e32 v182, v131, v183
	v_mul_f32_e32 v188, 0x3c000000, v182
	v_mul_f32_e32 v182, v132, v184
	v_mul_f32_e32 v184, 0x3c000000, v182
	v_add_f32_e32 v182, 1.0, v159
	v_mul_f32_e32 v5, v134, v5
	v_mul_f32_e32 v181, v135, v181
	v_rcp_f32_e32 v189, v182
	v_mul_f32_e32 v5, 0x3c000000, v5
	v_mul_f32_e32 v181, 0x3c000000, v181
	v_mov_b32_e32 v182, 0
	v_mov_b32_e32 v183, 0
	v_cvt_pk_fp8_f32 v182, v5, v181
	v_cvt_pk_fp8_f32 v183, v187, v188
	v_mul_f32_e32 v5, v133, v189
	v_mul_f32_e32 v5, 0x3c000000, v5
	v_cvt_pk_fp8_f32 v182, v185, v186 op_sel:[0,0,1]
	v_cvt_pk_fp8_f32 v183, v184, v5 op_sel:[0,0,1]
	s_mov_b64 s[58:59], 0
	ds_write_b64 v180, v[182:183]
.LBB0_563:
	s_andn2_b64 vcc, exec, s[58:59]
	v_lshl_add_u64 v[8:9], v[8:9], 1, s[38:39]
	s_cbranch_vccnz .LBB0_565
	global_load_dwordx4 v[182:185], v[8:9], off nt
	v_pk_add_f32 v[162:163], v[162:163], 1.0 op_sel_hi:[1,0]
	v_pk_add_f32 v[160:161], v[160:161], 1.0 op_sel_hi:[1,0]
	v_pk_add_f32 v[158:159], v[158:159], 1.0 op_sel_hi:[1,0]
	v_pk_add_f32 v[156:157], v[156:157], 1.0 op_sel_hi:[1,0]
	s_waitcnt vmcnt(0)
	v_lshlrev_b32_e32 v5, 16, v182
	v_and_b32_e32 v181, 0xffff0000, v182
	v_lshlrev_b32_e32 v182, 16, v183
	v_and_b32_e32 v183, 0xffff0000, v183
	v_lshlrev_b32_e32 v186, 16, v184
	v_and_b32_e32 v184, 0xffff0000, v184
	v_lshlrev_b32_e32 v187, 16, v185
	v_and_b32_e32 v185, 0xffff0000, v185
	v_mul_f32_e32 v5, 0xbfb8aa3b, v5
	v_mul_f32_e32 v181, 0xbfb8aa3b, v181
	v_mul_f32_e32 v182, 0xbfb8aa3b, v182
	v_mul_f32_e32 v183, 0xbfb8aa3b, v183
	v_mul_f32_e32 v186, 0xbfb8aa3b, v186
	v_mul_f32_e32 v184, 0xbfb8aa3b, v184
	v_mul_f32_e32 v187, 0xbfb8aa3b, v187
	v_mul_f32_e32 v185, 0xbfb8aa3b, v185
	v_exp_f32_e32 v5, v5
	v_exp_f32_e32 v181, v181
	v_exp_f32_e32 v182, v182
	v_exp_f32_e32 v183, v183
	v_exp_f32_e32 v186, v186
	v_exp_f32_e32 v184, v184
	v_exp_f32_e32 v187, v187
	v_exp_f32_e32 v185, v185
	v_add_f32_e32 v5, 1.0, v5
	v_add_f32_e32 v181, 1.0, v181
	v_add_f32_e32 v188, 1.0, v182
	v_add_f32_e32 v189, 1.0, v183
	v_add_f32_e32 v186, 1.0, v186
	v_add_f32_e32 v190, 1.0, v184
	v_add_f32_e32 v191, 1.0, v187
	v_add_f32_e32 v192, 1.0, v185
	v_rcp_f32_e32 v182, v5
	v_rcp_f32_e32 v183, v181
	v_rcp_f32_e32 v184, v188
	v_rcp_f32_e32 v185, v189
	v_rcp_f32_e32 v186, v186
	v_rcp_f32_e32 v187, v190
	v_rcp_f32_e32 v188, v191
	v_rcp_f32_e32 v189, v192
	v_pk_mul_f32 v[160:161], v[160:161], v[182:183]
	v_pk_mul_f32 v[162:163], v[162:163], v[184:185]
	v_pk_mul_f32 v[156:157], v[156:157], v[186:187]
	v_pk_mul_f32 v[158:159], v[158:159], v[188:189]
	v_pk_mul_f32 v[136:137], v[136:137], v[162:163]
	v_pk_mul_f32 v[134:135], v[134:135], v[160:161]
	v_pk_mul_f32 v[132:133], v[132:133], v[158:159]
	v_pk_mul_f32 v[130:131], v[130:131], v[156:157]
.LBB0_565:
	global_load_dwordx4 v[156:159], v[6:7], off offset:64 nt
	s_and_b64 vcc, exec, s[4:5]
	s_mov_b64 s[58:59], -1
	s_waitcnt vmcnt(0)
	v_lshlrev_b32_e32 v5, 16, v156
	v_and_b32_e32 v6, 0xffff0000, v156
	v_lshlrev_b32_e32 v7, 16, v157
	v_and_b32_e32 v156, 0xffff0000, v157
	v_lshlrev_b32_e32 v157, 16, v158
	v_and_b32_e32 v158, 0xffff0000, v158
	v_lshlrev_b32_e32 v160, 16, v159
	v_and_b32_e32 v159, 0xffff0000, v159
	v_mul_f32_e32 v5, 0xbfb8aa3b, v5
	v_mul_f32_e32 v6, 0xbfb8aa3b, v6
	v_mul_f32_e32 v7, 0xbfb8aa3b, v7
	v_mul_f32_e32 v156, 0xbfb8aa3b, v156
	v_mul_f32_e32 v157, 0xbfb8aa3b, v157
	v_mul_f32_e32 v162, 0xbfb8aa3b, v158
	v_mul_f32_e32 v163, 0xbfb8aa3b, v160
	v_mul_f32_e32 v181, 0xbfb8aa3b, v159
	v_exp_f32_e32 v158, v5
	v_exp_f32_e32 v159, v6
	v_exp_f32_e32 v160, v7
	v_exp_f32_e32 v161, v156
	v_exp_f32_e32 v6, v157
	v_exp_f32_e32 v7, v162
	v_exp_f32_e32 v156, v163
	v_exp_f32_e32 v157, v181
	s_cbranch_vccnz .LBB0_624
	v_add_f32_e32 v162, 1.0, v159
	v_add_f32_e32 v163, 1.0, v160
	v_rcp_f32_e32 v162, v162
	v_rcp_f32_e32 v163, v163
	v_add_f32_e32 v182, 1.0, v6
	v_rcp_f32_e32 v182, v182
	v_mul_f32_e32 v162, v103, v162
	v_mul_f32_e32 v181, 0x3c000000, v162
	v_mul_f32_e32 v162, v104, v163
	v_add_f32_e32 v163, 1.0, v161
	v_rcp_f32_e32 v163, v163
	v_mul_f32_e32 v183, 0x3c000000, v162
	v_add_f32_e32 v5, 1.0, v158
	v_rcp_f32_e32 v5, v5
	v_mul_f32_e32 v162, v105, v163
	v_add_f32_e32 v163, 1.0, v7
	v_mul_f32_e32 v184, 0x3c000000, v162
	v_mul_f32_e32 v162, v98, v182
	v_rcp_f32_e32 v163, v163
	v_add_f32_e32 v182, 1.0, v156
	v_rcp_f32_e32 v182, v182
	v_mul_f32_e32 v185, 0x3c000000, v162
	v_mul_f32_e32 v162, v99, v163
	v_mul_f32_e32 v186, 0x3c000000, v162
	v_mul_f32_e32 v162, v100, v182
	v_mul_f32_e32 v182, 0x3c000000, v162
	v_add_f32_e32 v162, 1.0, v157
	v_mul_f32_e32 v5, v102, v5
	v_rcp_f32_e32 v187, v162
	v_mul_f32_e32 v5, 0x3c000000, v5
	v_mov_b32_e32 v162, 0
	v_mov_b32_e32 v163, 0
	v_cvt_pk_fp8_f32 v162, v5, v181
	v_cvt_pk_fp8_f32 v163, v185, v186
	v_mul_f32_e32 v5, v101, v187
	v_mul_f32_e32 v5, 0x3c000000, v5
	v_cvt_pk_fp8_f32 v162, v183, v184 op_sel:[0,0,1]
	v_cvt_pk_fp8_f32 v163, v182, v5 op_sel:[0,0,1]
	ds_write_b64 v180, v[162:163] offset:32
	s_cbranch_execz .LBB0_625

; #define LAS __attribute__((address_space(3)))
; __device__ __forceinline__ unsigned pk4_fp8(float a, float b, float c, float d) { int w = 0; w = __builtin_amdgcn_cvt_pk_fp8_f32(a, b, w, false); w = __builtin_amdgcn_cvt_pk_fp8_f32(c, d, w, true); return (unsigned)w; }
; __device__ __forceinline__ float bf_lo(unsigned w) { return __uint_as_float(w << 16); }
; __device__ __forceinline__ float bf_hi(unsigned w) { return __uint_as_float(w & 0xffff0000u); }
; __device__ __forceinline__ float sigmoidf_fast(float x) { return __builtin_amdgcn_rcpf(1.0f + __builtin_amdgcn_exp2f(-1.4426950408889634f * x)); }
;     __device__ __forceinline__ void operator()(f32x4 (&acc)[2][2][4][2], const Unit& u, int wr, int wc, int fr, int fq) const {
;     ...
;                 const size_t ro = (size_t)(u.row0 + ai * 128 + wr * 64 + m * 16 + fr) * DM + col0;
; #pragma unroll
;                 for (int bj = 0; bj < 2; ++bj) {
;                     const u32x4 gd = *(const u32x4*)(GDF + ro + bj * 32);
;                     const float ed[8] = {bf_lo(gd.x), bf_hi(gd.x), bf_lo(gd.y), bf_hi(gd.y), bf_lo(gd.z), bf_hi(gd.z), bf_lo(gd.w), bf_hi(gd.w)};
;                     if (u.tag == 0) {
;                         const u32x4 gn = *(const u32x4*)(GNA + ro + bj * 32);
;                         const float en[8] = {bf_lo(gn.x), bf_hi(gn.x), bf_lo(gn.y), bf_hi(gn.y), bf_lo(gn.z), bf_hi(gn.z), bf_lo(gn.w), bf_hi(gn.w)};
; #pragma unroll
;                         for (int e = 0; e < 8; ++e) {
;                             const float r = (1.0f + __builtin_amdgcn_exp2f(-1.4426950408889634f * ed[e])) * __builtin_amdgcn_rcpf(1.0f + __builtin_amdgcn_exp2f(-1.4426950408889634f * en[e]));
;                             acc[ai][bj][m][e >> 2][e & 3] *= r; }
;                     } else {
;                         float y[8];
; #pragma unroll
;                         for (int e = 0; e < 8; ++e) y[e] = acc[ai][bj][m][e >> 2][e & 3] * sigmoidf_fast(ed[e]) * (PSCALE * WSCALE_INV * OSCALE_INV);
;                         u32x2 w; w.x = pk4_fp8(y[0], y[1], y[2], y[3]); w.y = pk4_fp8(y[4], y[5], y[6], y[7]);
;                         *(LAS u32x2*)(my + fr * 80 + bj * 32 + fq * 8) = w;
;                     }
.LBB0_569:
	s_nop 1
	v_add_u32_e32 v6, s76, v168
	v_ashrrev_i32_e32 v7, 31, v6
	v_lshlrev_b64 v[6:7], 11, v[6:7]
	v_lshl_add_u64 v[6:7], v[6:7], 0, v[2:3]
	v_lshl_add_u64 v[8:9], v[6:7], 1, s[40:41]
	global_load_dwordx4 v[156:159], v[8:9], off nt
	s_and_b64 vcc, exec, s[4:5]
	s_mov_b64 s[58:59], -1
	s_waitcnt vmcnt(0)
	v_lshlrev_b32_e32 v5, 16, v156
	v_and_b32_e32 v156, 0xffff0000, v156
	v_lshlrev_b32_e32 v160, 16, v157
	v_and_b32_e32 v157, 0xffff0000, v157
	v_lshlrev_b32_e32 v161, 16, v158
	v_and_b32_e32 v158, 0xffff0000, v158
	v_lshlrev_b32_e32 v162, 16, v159
	v_and_b32_e32 v159, 0xffff0000, v159
	v_mul_f32_e32 v5, 0xbfb8aa3b, v5
	v_mul_f32_e32 v156, 0xbfb8aa3b, v156
	v_mul_f32_e32 v163, 0xbfb8aa3b, v160
	v_mul_f32_e32 v157, 0xbfb8aa3b, v157
	v_mul_f32_e32 v181, 0xbfb8aa3b, v161
	v_mul_f32_e32 v158, 0xbfb8aa3b, v158
	v_mul_f32_e32 v182, 0xbfb8aa3b, v162
	v_mul_f32_e32 v159, 0xbfb8aa3b, v159
	v_exp_f32_e32 v160, v5
	v_exp_f32_e32 v161, v156
	v_exp_f32_e32 v162, v163
	v_exp_f32_e32 v163, v157
	v_exp_f32_e32 v156, v181
	v_exp_f32_e32 v157, v158
	v_exp_f32_e32 v158, v182
	v_exp_f32_e32 v159, v159
	s_cbranch_vccnz .LBB0_571
	v_add_f32_e32 v182, 1.0, v162
	v_rcp_f32_e32 v182, v182
	v_add_f32_e32 v183, 1.0, v163
	v_rcp_f32_e32 v183, v183
	v_add_f32_e32 v184, 1.0, v156
	v_rcp_f32_e32 v184, v184
	v_mul_f32_e32 v182, v128, v182
	v_mul_f32_e32 v185, 0x3c000000, v182
	v_mul_f32_e32 v182, v129, v183
	v_add_f32_e32 v183, 1.0, v157
	v_mul_f32_e32 v186, 0x3c000000, v182
	v_mul_f32_e32 v182, v122, v184
	v_rcp_f32_e32 v183, v183
	v_add_f32_e32 v184, 1.0, v158
	v_rcp_f32_e32 v184, v184
	v_add_f32_e32 v5, 1.0, v160
	v_add_f32_e32 v181, 1.0, v161
	v_rcp_f32_e32 v5, v5
	v_rcp_f32_e32 v181, v181
	v_mul_f32_e32 v187, 0x3c000000, v182
	v_mul_f32_e32 v182, v123, v183
	v_mul_f32_e32 v188, 0x3c000000, v182
	v_mul_f32_e32 v182, v124, v184
	v_mul_f32_e32 v184, 0x3c000000, v182
	v_add_f32_e32 v182, 1.0, v159
	v_mul_f32_e32 v5, v126, v5
	v_mul_f32_e32 v181, v127, v181
	v_rcp_f32_e32 v189, v182
	v_mul_f32_e32 v5, 0x3c000000, v5
	v_mul_f32_e32 v181, 0x3c000000, v181
	v_mov_b32_e32 v182, 0
	v_mov_b32_e32 v183, 0
	v_cvt_pk_fp8_f32 v182, v5, v181
	v_cvt_pk_fp8_f32 v183, v187, v188
	v_mul_f32_e32 v5, v125, v189
	v_mul_f32_e32 v5, 0x3c000000, v5
	v_cvt_pk_fp8_f32 v182, v185, v186 op_sel:[0,0,1]
	v_cvt_pk_fp8_f32 v183, v184, v5 op_sel:[0,0,1]
	s_mov_b64 s[58:59], 0
	ds_write_b64 v180, v[182:183]
.LBB0_571:
	s_andn2_b64 vcc, exec, s[58:59]
	v_lshl_add_u64 v[6:7], v[6:7], 1, s[38:39]
	s_cbranch_vccnz .LBB0_573
	global_load_dwordx4 v[182:185], v[6:7], off nt
	v_pk_add_f32 v[162:163], v[162:163], 1.0 op_sel_hi:[1,0]
	v_pk_add_f32 v[160:161], v[160:161], 1.0 op_sel_hi:[1,0]
	v_pk_add_f32 v[158:159], v[158:159], 1.0 op_sel_hi:[1,0]
	v_pk_add_f32 v[156:157], v[156:157], 1.0 op_sel_hi:[1,0]
	s_waitcnt vmcnt(0)
	v_lshlrev_b32_e32 v5, 16, v182
	v_and_b32_e32 v181, 0xffff0000, v182
	v_lshlrev_b32_e32 v182, 16, v183
	v_and_b32_e32 v183, 0xffff0000, v183
	v_lshlrev_b32_e32 v186, 16, v184
	v_and_b32_e32 v184, 0xffff0000, v184
	v_lshlrev_b32_e32 v187, 16, v185
	v_and_b32_e32 v185, 0xffff0000, v185
	v_mul_f32_e32 v5, 0xbfb8aa3b, v5
	v_mul_f32_e32 v181, 0xbfb8aa3b, v181
	v_mul_f32_e32 v182, 0xbfb8aa3b, v182
	v_mul_f32_e32 v183, 0xbfb8aa3b, v183
	v_mul_f32_e32 v186, 0xbfb8aa3b, v186
	v_mul_f32_e32 v184, 0xbfb8aa3b, v184
	v_mul_f32_e32 v187, 0xbfb8aa3b, v187
	v_mul_f32_e32 v185, 0xbfb8aa3b, v185
	v_exp_f32_e32 v5, v5
	v_exp_f32_e32 v181, v181
	v_exp_f32_e32 v182, v182
	v_exp_f32_e32 v183, v183
	v_exp_f32_e32 v186, v186
	v_exp_f32_e32 v184, v184
	v_exp_f32_e32 v187, v187
	v_exp_f32_e32 v185, v185
	v_add_f32_e32 v5, 1.0, v5
	v_add_f32_e32 v181, 1.0, v181
	v_add_f32_e32 v188, 1.0, v182
	v_add_f32_e32 v189, 1.0, v183
	v_add_f32_e32 v186, 1.0, v186
	v_add_f32_e32 v190, 1.0, v184
	v_add_f32_e32 v191, 1.0, v187
	v_add_f32_e32 v192, 1.0, v185
	v_rcp_f32_e32 v182, v5
	v_rcp_f32_e32 v183, v181
	v_rcp_f32_e32 v184, v188
	v_rcp_f32_e32 v185, v189
	v_rcp_f32_e32 v186, v186
	v_rcp_f32_e32 v187, v190
	v_rcp_f32_e32 v188, v191
	v_rcp_f32_e32 v189, v192
	v_pk_mul_f32 v[160:161], v[160:161], v[182:183]
	v_pk_mul_f32 v[162:163], v[162:163], v[184:185]
	v_pk_mul_f32 v[156:157], v[156:157], v[186:187]
	v_pk_mul_f32 v[158:159], v[158:159], v[188:189]
	v_pk_mul_f32 v[128:129], v[128:129], v[162:163]
	v_pk_mul_f32 v[126:127], v[126:127], v[160:161]
	v_pk_mul_f32 v[124:125], v[124:125], v[158:159]
	v_pk_mul_f32 v[122:123], v[122:123], v[156:157]
.LBB0_573:
	global_load_dwordx4 v[156:159], v[8:9], off offset:64 nt
	s_and_b64 vcc, exec, s[4:5]
	s_mov_b64 s[58:59], -1
	s_waitcnt vmcnt(0)
	v_lshlrev_b32_e32 v5, 16, v156
	v_and_b32_e32 v8, 0xffff0000, v156
	v_lshlrev_b32_e32 v9, 16, v157
	v_and_b32_e32 v156, 0xffff0000, v157
	v_lshlrev_b32_e32 v157, 16, v158
	v_and_b32_e32 v158, 0xffff0000, v158
	v_lshlrev_b32_e32 v160, 16, v159
	v_and_b32_e32 v159, 0xffff0000, v159
	v_mul_f32_e32 v5, 0xbfb8aa3b, v5
	v_mul_f32_e32 v8, 0xbfb8aa3b, v8
	v_mul_f32_e32 v9, 0xbfb8aa3b, v9
	v_mul_f32_e32 v156, 0xbfb8aa3b, v156
	v_mul_f32_e32 v157, 0xbfb8aa3b, v157
	v_mul_f32_e32 v162, 0xbfb8aa3b, v158
	v_mul_f32_e32 v163, 0xbfb8aa3b, v160
	v_mul_f32_e32 v181, 0xbfb8aa3b, v159
	v_exp_f32_e32 v158, v5
	v_exp_f32_e32 v159, v8
	v_exp_f32_e32 v160, v9
	v_exp_f32_e32 v161, v156
	v_exp_f32_e32 v8, v157
	v_exp_f32_e32 v9, v162
	v_exp_f32_e32 v156, v163
	v_exp_f32_e32 v157, v181
	s_cbranch_vccnz .LBB0_626
	v_add_f32_e32 v162, 1.0, v159
	v_add_f32_e32 v163, 1.0, v160
	v_rcp_f32_e32 v162, v162
	v_rcp_f32_e32 v163, v163
	v_add_f32_e32 v182, 1.0, v8
	v_rcp_f32_e32 v182, v182
	v_mul_f32_e32 v162, v95, v162
	v_mul_f32_e32 v181, 0x3c000000, v162
	v_mul_f32_e32 v162, v96, v163
	v_add_f32_e32 v163, 1.0, v161
	v_rcp_f32_e32 v163, v163
	v_mul_f32_e32 v183, 0x3c000000, v162
	v_add_f32_e32 v5, 1.0, v158
	v_rcp_f32_e32 v5, v5
	v_mul_f32_e32 v162, v97, v163
	v_add_f32_e32 v163, 1.0, v9
	v_mul_f32_e32 v184, 0x3c000000, v162
	v_mul_f32_e32 v162, v90, v182
	v_rcp_f32_e32 v163, v163
	v_add_f32_e32 v182, 1.0, v156
	v_rcp_f32_e32 v182, v182
	v_mul_f32_e32 v185, 0x3c000000, v162
	v_mul_f32_e32 v162, v91, v163
	v_mul_f32_e32 v186, 0x3c000000, v162
	v_mul_f32_e32 v162, v92, v182
	v_mul_f32_e32 v182, 0x3c000000, v162
	v_add_f32_e32 v162, 1.0, v157
	v_mul_f32_e32 v5, v94, v5
	v_rcp_f32_e32 v187, v162
	v_mul_f32_e32 v5, 0x3c000000, v5
	v_mov_b32_e32 v162, 0
	v_mov_b32_e32 v163, 0
	v_cvt_pk_fp8_f32 v162, v5, v181
	v_cvt_pk_fp8_f32 v163, v185, v186
	v_mul_f32_e32 v5, v93, v187
	v_mul_f32_e32 v5, 0x3c000000, v5
	v_cvt_pk_fp8_f32 v162, v183, v184 op_sel:[0,0,1]
	v_cvt_pk_fp8_f32 v163, v182, v5 op_sel:[0,0,1]
	ds_write_b64 v180, v[162:163] offset:32
	s_cbranch_execz .LBB0_627

; #define LAS __attribute__((address_space(3)))
; __device__ __forceinline__ unsigned pk4_fp8(float a, float b, float c, float d) { int w = 0; w = __builtin_amdgcn_cvt_pk_fp8_f32(a, b, w, false); w = __builtin_amdgcn_cvt_pk_fp8_f32(c, d, w, true); return (unsigned)w; }
; __device__ __forceinline__ float bf_lo(unsigned w) { return __uint_as_float(w << 16); }
; __device__ __forceinline__ float bf_hi(unsigned w) { return __uint_as_float(w & 0xffff0000u); }
; __device__ __forceinline__ float sigmoidf_fast(float x) { return __builtin_amdgcn_rcpf(1.0f + __builtin_amdgcn_exp2f(-1.4426950408889634f * x)); }
;     __device__ __forceinline__ void operator()(f32x4 (&acc)[2][2][4][2], const Unit& u, int wr, int wc, int fr, int fq) const {
;     ...
;                 const size_t ro = (size_t)(u.row0 + ai * 128 + wr * 64 + m * 16 + fr) * DM + col0;
; #pragma unroll
;                 for (int bj = 0; bj < 2; ++bj) {
;                     const u32x4 gd = *(const u32x4*)(GDF + ro + bj * 32);
;                     const float ed[8] = {bf_lo(gd.x), bf_hi(gd.x), bf_lo(gd.y), bf_hi(gd.y), bf_lo(gd.z), bf_hi(gd.z), bf_lo(gd.w), bf_hi(gd.w)};
;                     if (u.tag == 0) {
;                         const u32x4 gn = *(const u32x4*)(GNA + ro + bj * 32);
;                         const float en[8] = {bf_lo(gn.x), bf_hi(gn.x), bf_lo(gn.y), bf_hi(gn.y), bf_lo(gn.z), bf_hi(gn.z), bf_lo(gn.w), bf_hi(gn.w)};
; #pragma unroll
;                         for (int e = 0; e < 8; ++e) {
;                             const float r = (1.0f + __builtin_amdgcn_exp2f(-1.4426950408889634f * ed[e])) * __builtin_amdgcn_rcpf(1.0f + __builtin_amdgcn_exp2f(-1.4426950408889634f * en[e]));
;                             acc[ai][bj][m][e >> 2][e & 3] *= r; }
;                     } else {
;                         float y[8];
; #pragma unroll
;                         for (int e = 0; e < 8; ++e) y[e] = acc[ai][bj][m][e >> 2][e & 3] * sigmoidf_fast(ed[e]) * (PSCALE * WSCALE_INV * OSCALE_INV);
;                         u32x2 w; w.x = pk4_fp8(y[0], y[1], y[2], y[3]); w.y = pk4_fp8(y[4], y[5], y[6], y[7]);
;                         *(LAS u32x2*)(my + fr * 80 + bj * 32 + fq * 8) = w;
;                     }
.LBB0_577:
	s_nop 1
	v_add_u32_e32 v6, s76, v171
	v_ashrrev_i32_e32 v7, 31, v6
	v_lshlrev_b64 v[6:7], 11, v[6:7]
	v_lshl_add_u64 v[6:7], v[6:7], 0, v[2:3]
	v_lshl_add_u64 v[8:9], v[6:7], 1, s[40:41]
	global_load_dwordx4 v[156:159], v[8:9], off nt
	s_and_b64 vcc, exec, s[4:5]
	s_mov_b64 s[58:59], -1
	s_waitcnt vmcnt(0)
	v_lshlrev_b32_e32 v5, 16, v156
	v_and_b32_e32 v156, 0xffff0000, v156
	v_lshlrev_b32_e32 v160, 16, v157
	v_and_b32_e32 v157, 0xffff0000, v157
	v_lshlrev_b32_e32 v161, 16, v158
	v_and_b32_e32 v158, 0xffff0000, v158
	v_lshlrev_b32_e32 v162, 16, v159
	v_and_b32_e32 v159, 0xffff0000, v159
	v_mul_f32_e32 v5, 0xbfb8aa3b, v5
	v_mul_f32_e32 v156, 0xbfb8aa3b, v156
	v_mul_f32_e32 v163, 0xbfb8aa3b, v160
	v_mul_f32_e32 v157, 0xbfb8aa3b, v157
	v_mul_f32_e32 v181, 0xbfb8aa3b, v161
	v_mul_f32_e32 v158, 0xbfb8aa3b, v158
	v_mul_f32_e32 v182, 0xbfb8aa3b, v162
	v_mul_f32_e32 v159, 0xbfb8aa3b, v159
	v_exp_f32_e32 v160, v5
	v_exp_f32_e32 v161, v156
	v_exp_f32_e32 v162, v163
	v_exp_f32_e32 v163, v157
	v_exp_f32_e32 v156, v181
	v_exp_f32_e32 v157, v158
	v_exp_f32_e32 v158, v182
	v_exp_f32_e32 v159, v159
	s_cbranch_vccnz .LBB0_579
	v_add_f32_e32 v182, 1.0, v162
	v_rcp_f32_e32 v182, v182
	v_add_f32_e32 v183, 1.0, v163
	v_rcp_f32_e32 v183, v183
	v_add_f32_e32 v184, 1.0, v156
	v_rcp_f32_e32 v184, v184
	v_mul_f32_e32 v182, v120, v182
	v_mul_f32_e32 v185, 0x3c000000, v182
	v_mul_f32_e32 v182, v121, v183
	v_add_f32_e32 v183, 1.0, v157
	v_mul_f32_e32 v186, 0x3c000000, v182
	v_mul_f32_e32 v182, v114, v184
	v_rcp_f32_e32 v183, v183
	v_add_f32_e32 v184, 1.0, v158
	v_rcp_f32_e32 v184, v184
	v_add_f32_e32 v5, 1.0, v160
	v_add_f32_e32 v181, 1.0, v161
	v_rcp_f32_e32 v5, v5
	v_rcp_f32_e32 v181, v181
	v_mul_f32_e32 v187, 0x3c000000, v182
	v_mul_f32_e32 v182, v115, v183
	v_mul_f32_e32 v188, 0x3c000000, v182
	v_mul_f32_e32 v182, v116, v184
	v_mul_f32_e32 v184, 0x3c000000, v182
	v_add_f32_e32 v182, 1.0, v159
	v_mul_f32_e32 v5, v118, v5
	v_mul_f32_e32 v181, v119, v181
	v_rcp_f32_e32 v189, v182
	v_mul_f32_e32 v5, 0x3c000000, v5
	v_mul_f32_e32 v181, 0x3c000000, v181
	v_mov_b32_e32 v182, 0
	v_mov_b32_e32 v183, 0
	v_cvt_pk_fp8_f32 v182, v5, v181
	v_cvt_pk_fp8_f32 v183, v187, v188
	v_mul_f32_e32 v5, v117, v189
	v_mul_f32_e32 v5, 0x3c000000, v5
	v_cvt_pk_fp8_f32 v182, v185, v186 op_sel:[0,0,1]
	v_cvt_pk_fp8_f32 v183, v184, v5 op_sel:[0,0,1]
	s_mov_b64 s[58:59], 0
	ds_write_b64 v180, v[182:183]
.LBB0_579:
	s_andn2_b64 vcc, exec, s[58:59]
	v_lshl_add_u64 v[6:7], v[6:7], 1, s[38:39]
	s_cbranch_vccnz .LBB0_581
	global_load_dwordx4 v[182:185], v[6:7], off nt
	v_pk_add_f32 v[162:163], v[162:163], 1.0 op_sel_hi:[1,0]
	v_pk_add_f32 v[160:161], v[160:161], 1.0 op_sel_hi:[1,0]
	v_pk_add_f32 v[158:159], v[158:159], 1.0 op_sel_hi:[1,0]
	v_pk_add_f32 v[156:157], v[156:157], 1.0 op_sel_hi:[1,0]
	s_waitcnt vmcnt(0)
	v_lshlrev_b32_e32 v5, 16, v182
	v_and_b32_e32 v181, 0xffff0000, v182
	v_lshlrev_b32_e32 v182, 16, v183
	v_and_b32_e32 v183, 0xffff0000, v183
	v_lshlrev_b32_e32 v186, 16, v184
	v_and_b32_e32 v184, 0xffff0000, v184
	v_lshlrev_b32_e32 v187, 16, v185
	v_and_b32_e32 v185, 0xffff0000, v185
	v_mul_f32_e32 v5, 0xbfb8aa3b, v5
	v_mul_f32_e32 v181, 0xbfb8aa3b, v181
	v_mul_f32_e32 v182, 0xbfb8aa3b, v182
	v_mul_f32_e32 v183, 0xbfb8aa3b, v183
	v_mul_f32_e32 v186, 0xbfb8aa3b, v186
	v_mul_f32_e32 v184, 0xbfb8aa3b, v184
	v_mul_f32_e32 v187, 0xbfb8aa3b, v187
	v_mul_f32_e32 v185, 0xbfb8aa3b, v185
	v_exp_f32_e32 v5, v5
	v_exp_f32_e32 v181, v181
	v_exp_f32_e32 v182, v182
	v_exp_f32_e32 v183, v183
	v_exp_f32_e32 v186, v186
	v_exp_f32_e32 v184, v184
	v_exp_f32_e32 v187, v187
	v_exp_f32_e32 v185, v185
	v_add_f32_e32 v5, 1.0, v5
	v_add_f32_e32 v181, 1.0, v181
	v_add_f32_e32 v188, 1.0, v182
	v_add_f32_e32 v189, 1.0, v183
	v_add_f32_e32 v186, 1.0, v186
	v_add_f32_e32 v190, 1.0, v184
	v_add_f32_e32 v191, 1.0, v187
	v_add_f32_e32 v192, 1.0, v185
	v_rcp_f32_e32 v182, v5
	v_rcp_f32_e32 v183, v181
	v_rcp_f32_e32 v184, v188
	v_rcp_f32_e32 v185, v189
	v_rcp_f32_e32 v186, v186
	v_rcp_f32_e32 v187, v190
	v_rcp_f32_e32 v188, v191
	v_rcp_f32_e32 v189, v192
	v_pk_mul_f32 v[160:161], v[160:161], v[182:183]
	v_pk_mul_f32 v[162:163], v[162:163], v[184:185]
	v_pk_mul_f32 v[156:157], v[156:157], v[186:187]
	v_pk_mul_f32 v[158:159], v[158:159], v[188:189]
	v_pk_mul_f32 v[120:121], v[120:121], v[162:163]
	v_pk_mul_f32 v[118:119], v[118:119], v[160:161]
	v_pk_mul_f32 v[116:117], v[116:117], v[158:159]
	v_pk_mul_f32 v[114:115], v[114:115], v[156:157]
.LBB0_581:
	global_load_dwordx4 v[156:159], v[8:9], off offset:64 nt
	s_and_b64 vcc, exec, s[4:5]
	s_mov_b64 s[58:59], -1
	s_waitcnt vmcnt(0)
	v_lshlrev_b32_e32 v5, 16, v156
	v_and_b32_e32 v8, 0xffff0000, v156
	v_lshlrev_b32_e32 v9, 16, v157
	v_and_b32_e32 v156, 0xffff0000, v157
	v_lshlrev_b32_e32 v157, 16, v158
	v_and_b32_e32 v158, 0xffff0000, v158
	v_lshlrev_b32_e32 v160, 16, v159
	v_and_b32_e32 v159, 0xffff0000, v159
	v_mul_f32_e32 v5, 0xbfb8aa3b, v5
	v_mul_f32_e32 v8, 0xbfb8aa3b, v8
	v_mul_f32_e32 v9, 0xbfb8aa3b, v9
	v_mul_f32_e32 v156, 0xbfb8aa3b, v156
	v_mul_f32_e32 v157, 0xbfb8aa3b, v157
	v_mul_f32_e32 v162, 0xbfb8aa3b, v158
	v_mul_f32_e32 v163, 0xbfb8aa3b, v160
	v_mul_f32_e32 v181, 0xbfb8aa3b, v159
	v_exp_f32_e32 v158, v5
	v_exp_f32_e32 v159, v8
	v_exp_f32_e32 v160, v9
	v_exp_f32_e32 v161, v156
	v_exp_f32_e32 v8, v157
	v_exp_f32_e32 v9, v162
	v_exp_f32_e32 v156, v163
	v_exp_f32_e32 v157, v181
	s_cbranch_vccnz .LBB0_628
	v_add_f32_e32 v162, 1.0, v159
	v_add_f32_e32 v163, 1.0, v160
	v_rcp_f32_e32 v162, v162
	v_rcp_f32_e32 v163, v163
	v_add_f32_e32 v182, 1.0, v8
	v_rcp_f32_e32 v182, v182
	v_mul_f32_e32 v162, v87, v162
	v_mul_f32_e32 v181, 0x3c000000, v162
	v_mul_f32_e32 v162, v88, v163
	v_add_f32_e32 v163, 1.0, v161
	v_rcp_f32_e32 v163, v163
	v_mul_f32_e32 v183, 0x3c000000, v162
	v_add_f32_e32 v5, 1.0, v158
	v_rcp_f32_e32 v5, v5
	v_mul_f32_e32 v162, v89, v163
	v_add_f32_e32 v163, 1.0, v9
	v_mul_f32_e32 v184, 0x3c000000, v162
	v_mul_f32_e32 v162, v82, v182
	v_rcp_f32_e32 v163, v163
	v_add_f32_e32 v182, 1.0, v156
	v_rcp_f32_e32 v182, v182
	v_mul_f32_e32 v185, 0x3c000000, v162
	v_mul_f32_e32 v162, v83, v163
	v_mul_f32_e32 v186, 0x3c000000, v162
	v_mul_f32_e32 v162, v84, v182
	v_mul_f32_e32 v182, 0x3c000000, v162
	v_add_f32_e32 v162, 1.0, v157
	v_mul_f32_e32 v5, v86, v5
	v_rcp_f32_e32 v187, v162
	v_mul_f32_e32 v5, 0x3c000000, v5
	v_mov_b32_e32 v162, 0
	v_mov_b32_e32 v163, 0
	v_cvt_pk_fp8_f32 v162, v5, v181
	v_cvt_pk_fp8_f32 v163, v185, v186
	v_mul_f32_e32 v5, v85, v187
	v_mul_f32_e32 v5, 0x3c000000, v5
	v_cvt_pk_fp8_f32 v162, v183, v184 op_sel:[0,0,1]
	v_cvt_pk_fp8_f32 v163, v182, v5 op_sel:[0,0,1]
	ds_write_b64 v180, v[162:163] offset:32
	s_cbranch_execz .LBB0_629

; #define LAS __attribute__((address_space(3)))
; __device__ __forceinline__ unsigned pk4_fp8(float a, float b, float c, float d) { int w = 0; w = __builtin_amdgcn_cvt_pk_fp8_f32(a, b, w, false); w = __builtin_amdgcn_cvt_pk_fp8_f32(c, d, w, true); return (unsigned)w; }
; __device__ __forceinline__ float bf_lo(unsigned w) { return __uint_as_float(w << 16); }
; __device__ __forceinline__ float bf_hi(unsigned w) { return __uint_as_float(w & 0xffff0000u); }
; __device__ __forceinline__ float sigmoidf_fast(float x) { return __builtin_amdgcn_rcpf(1.0f + __builtin_amdgcn_exp2f(-1.4426950408889634f * x)); }
;     __device__ __forceinline__ void operator()(f32x4 (&acc)[2][2][4][2], const Unit& u, int wr, int wc, int fr, int fq) const {
;     ...
;                 const size_t ro = (size_t)(u.row0 + ai * 128 + wr * 64 + m * 16 + fr) * DM + col0;
; #pragma unroll
;                 for (int bj = 0; bj < 2; ++bj) {
;                     const u32x4 gd = *(const u32x4*)(GDF + ro + bj * 32);
;                     const float ed[8] = {bf_lo(gd.x), bf_hi(gd.x), bf_lo(gd.y), bf_hi(gd.y), bf_lo(gd.z), bf_hi(gd.z), bf_lo(gd.w), bf_hi(gd.w)};
;                     if (u.tag == 0) {
;                         const u32x4 gn = *(const u32x4*)(GNA + ro + bj * 32);
;                         const float en[8] = {bf_lo(gn.x), bf_hi(gn.x), bf_lo(gn.y), bf_hi(gn.y), bf_lo(gn.z), bf_hi(gn.z), bf_lo(gn.w), bf_hi(gn.w)};
; #pragma unroll
;                         for (int e = 0; e < 8; ++e) {
;                             const float r = (1.0f + __builtin_amdgcn_exp2f(-1.4426950408889634f * ed[e])) * __builtin_amdgcn_rcpf(1.0f + __builtin_amdgcn_exp2f(-1.4426950408889634f * en[e]));
;                             acc[ai][bj][m][e >> 2][e & 3] *= r; }
;                     } else {
;                         float y[8];
; #pragma unroll
;                         for (int e = 0; e < 8; ++e) y[e] = acc[ai][bj][m][e >> 2][e & 3] * sigmoidf_fast(ed[e]) * (PSCALE * WSCALE_INV * OSCALE_INV);
;                         u32x2 w; w.x = pk4_fp8(y[0], y[1], y[2], y[3]); w.y = pk4_fp8(y[4], y[5], y[6], y[7]);
;                         *(LAS u32x2*)(my + fr * 80 + bj * 32 + fq * 8) = w;
;                     }
.LBB0_585:
	s_nop 1
	v_add_u32_e32 v6, s76, v173
	v_ashrrev_i32_e32 v7, 31, v6
	v_lshlrev_b64 v[6:7], 11, v[6:7]
	v_lshl_add_u64 v[6:7], v[6:7], 0, v[2:3]
	v_lshl_add_u64 v[8:9], v[6:7], 1, s[40:41]
	global_load_dwordx4 v[156:159], v[8:9], off nt
	s_and_b64 vcc, exec, s[4:5]
	s_mov_b64 s[58:59], -1
	s_waitcnt vmcnt(0)
	v_lshlrev_b32_e32 v5, 16, v156
	v_and_b32_e32 v156, 0xffff0000, v156
	v_lshlrev_b32_e32 v160, 16, v157
	v_and_b32_e32 v157, 0xffff0000, v157
	v_lshlrev_b32_e32 v161, 16, v158
	v_and_b32_e32 v158, 0xffff0000, v158
	v_lshlrev_b32_e32 v162, 16, v159
	v_and_b32_e32 v159, 0xffff0000, v159
	v_mul_f32_e32 v5, 0xbfb8aa3b, v5
	v_mul_f32_e32 v156, 0xbfb8aa3b, v156
	v_mul_f32_e32 v163, 0xbfb8aa3b, v160
	v_mul_f32_e32 v157, 0xbfb8aa3b, v157
	v_mul_f32_e32 v181, 0xbfb8aa3b, v161
	v_mul_f32_e32 v158, 0xbfb8aa3b, v158
	v_mul_f32_e32 v182, 0xbfb8aa3b, v162
	v_mul_f32_e32 v159, 0xbfb8aa3b, v159
	v_exp_f32_e32 v160, v5
	v_exp_f32_e32 v161, v156
	v_exp_f32_e32 v162, v163
	v_exp_f32_e32 v163, v157
	v_exp_f32_e32 v156, v181
	v_exp_f32_e32 v157, v158
	v_exp_f32_e32 v158, v182
	v_exp_f32_e32 v159, v159
	s_cbranch_vccnz .LBB0_587
	v_add_f32_e32 v182, 1.0, v162
	v_rcp_f32_e32 v182, v182
	v_add_f32_e32 v183, 1.0, v163
	v_rcp_f32_e32 v183, v183
	v_add_f32_e32 v184, 1.0, v156
	v_rcp_f32_e32 v184, v184
	v_mul_f32_e32 v182, v112, v182
	v_mul_f32_e32 v185, 0x3c000000, v182
	v_mul_f32_e32 v182, v113, v183
	v_add_f32_e32 v183, 1.0, v157
	v_mul_f32_e32 v186, 0x3c000000, v182
	v_mul_f32_e32 v182, v106, v184
	v_rcp_f32_e32 v183, v183
	v_add_f32_e32 v184, 1.0, v158
	v_rcp_f32_e32 v184, v184
	v_add_f32_e32 v5, 1.0, v160
	v_add_f32_e32 v181, 1.0, v161
	v_rcp_f32_e32 v5, v5
	v_rcp_f32_e32 v181, v181
	v_mul_f32_e32 v187, 0x3c000000, v182
	v_mul_f32_e32 v182, v107, v183
	v_mul_f32_e32 v188, 0x3c000000, v182
	v_mul_f32_e32 v182, v108, v184
	v_mul_f32_e32 v184, 0x3c000000, v182
	v_add_f32_e32 v182, 1.0, v159
	v_mul_f32_e32 v5, v110, v5
	v_mul_f32_e32 v181, v111, v181
	v_rcp_f32_e32 v189, v182
	v_mul_f32_e32 v5, 0x3c000000, v5
	v_mul_f32_e32 v181, 0x3c000000, v181
	v_mov_b32_e32 v182, 0
	v_mov_b32_e32 v183, 0
	v_cvt_pk_fp8_f32 v182, v5, v181
	v_cvt_pk_fp8_f32 v183, v187, v188
	v_mul_f32_e32 v5, v109, v189
	v_mul_f32_e32 v5, 0x3c000000, v5
	v_cvt_pk_fp8_f32 v182, v185, v186 op_sel:[0,0,1]
	v_cvt_pk_fp8_f32 v183, v184, v5 op_sel:[0,0,1]
	s_mov_b64 s[58:59], 0
	ds_write_b64 v180, v[182:183]
.LBB0_587:
	s_andn2_b64 vcc, exec, s[58:59]
	v_lshl_add_u64 v[6:7], v[6:7], 1, s[38:39]
	s_cbranch_vccnz .LBB0_589
	global_load_dwordx4 v[182:185], v[6:7], off nt
	v_pk_add_f32 v[162:163], v[162:163], 1.0 op_sel_hi:[1,0]
	v_pk_add_f32 v[160:161], v[160:161], 1.0 op_sel_hi:[1,0]
	v_pk_add_f32 v[158:159], v[158:159], 1.0 op_sel_hi:[1,0]
	v_pk_add_f32 v[156:157], v[156:157], 1.0 op_sel_hi:[1,0]
	s_waitcnt vmcnt(0)
	v_lshlrev_b32_e32 v5, 16, v182
	v_and_b32_e32 v181, 0xffff0000, v182
	v_lshlrev_b32_e32 v182, 16, v183
	v_and_b32_e32 v183, 0xffff0000, v183
	v_lshlrev_b32_e32 v186, 16, v184
	v_and_b32_e32 v184, 0xffff0000, v184
	v_lshlrev_b32_e32 v187, 16, v185
	v_and_b32_e32 v185, 0xffff0000, v185
	v_mul_f32_e32 v5, 0xbfb8aa3b, v5
	v_mul_f32_e32 v181, 0xbfb8aa3b, v181
	v_mul_f32_e32 v182, 0xbfb8aa3b, v182
	v_mul_f32_e32 v183, 0xbfb8aa3b, v183
	v_mul_f32_e32 v186, 0xbfb8aa3b, v186
	v_mul_f32_e32 v184, 0xbfb8aa3b, v184
	v_mul_f32_e32 v187, 0xbfb8aa3b, v187
	v_mul_f32_e32 v185, 0xbfb8aa3b, v185
	v_exp_f32_e32 v5, v5
	v_exp_f32_e32 v181, v181
	v_exp_f32_e32 v182, v182
	v_exp_f32_e32 v183, v183
	v_exp_f32_e32 v186, v186
	v_exp_f32_e32 v184, v184
	v_exp_f32_e32 v187, v187
	v_exp_f32_e32 v185, v185
	v_add_f32_e32 v5, 1.0, v5
	v_add_f32_e32 v181, 1.0, v181
	v_add_f32_e32 v188, 1.0, v182
	v_add_f32_e32 v189, 1.0, v183
	v_add_f32_e32 v186, 1.0, v186
	v_add_f32_e32 v190, 1.0, v184
	v_add_f32_e32 v191, 1.0, v187
	v_add_f32_e32 v192, 1.0, v185
	v_rcp_f32_e32 v182, v5
	v_rcp_f32_e32 v183, v181
	v_rcp_f32_e32 v184, v188
	v_rcp_f32_e32 v185, v189
	v_rcp_f32_e32 v186, v186
	v_rcp_f32_e32 v187, v190
	v_rcp_f32_e32 v188, v191
	v_rcp_f32_e32 v189, v192
	v_pk_mul_f32 v[160:161], v[160:161], v[182:183]
	v_pk_mul_f32 v[162:163], v[162:163], v[184:185]
	v_pk_mul_f32 v[156:157], v[156:157], v[186:187]
	v_pk_mul_f32 v[158:159], v[158:159], v[188:189]
	v_pk_mul_f32 v[112:113], v[112:113], v[162:163]
	v_pk_mul_f32 v[110:111], v[110:111], v[160:161]
	v_pk_mul_f32 v[108:109], v[108:109], v[158:159]
	v_pk_mul_f32 v[106:107], v[106:107], v[156:157]
.LBB0_589:
	global_load_dwordx4 v[156:159], v[8:9], off offset:64 nt
	s_and_b64 vcc, exec, s[4:5]
	s_mov_b64 s[58:59], -1
	s_waitcnt vmcnt(0)
	v_lshlrev_b32_e32 v5, 16, v156
	v_and_b32_e32 v8, 0xffff0000, v156
	v_lshlrev_b32_e32 v9, 16, v157
	v_and_b32_e32 v156, 0xffff0000, v157
	v_lshlrev_b32_e32 v157, 16, v158
	v_and_b32_e32 v158, 0xffff0000, v158
	v_lshlrev_b32_e32 v160, 16, v159
	v_and_b32_e32 v159, 0xffff0000, v159
	v_mul_f32_e32 v5, 0xbfb8aa3b, v5
	v_mul_f32_e32 v8, 0xbfb8aa3b, v8
	v_mul_f32_e32 v9, 0xbfb8aa3b, v9
	v_mul_f32_e32 v156, 0xbfb8aa3b, v156
	v_mul_f32_e32 v157, 0xbfb8aa3b, v157
	v_mul_f32_e32 v162, 0xbfb8aa3b, v158
	v_mul_f32_e32 v163, 0xbfb8aa3b, v160
	v_mul_f32_e32 v181, 0xbfb8aa3b, v159
	v_exp_f32_e32 v158, v5
	v_exp_f32_e32 v159, v8
	v_exp_f32_e32 v160, v9
	v_exp_f32_e32 v161, v156
	v_exp_f32_e32 v8, v157
	v_exp_f32_e32 v9, v162
	v_exp_f32_e32 v156, v163
	v_exp_f32_e32 v157, v181
	s_cbranch_vccnz .LBB0_630
	v_add_f32_e32 v162, 1.0, v159
	v_add_f32_e32 v163, 1.0, v160
	v_rcp_f32_e32 v162, v162
	v_rcp_f32_e32 v163, v163
	v_add_f32_e32 v182, 1.0, v8
	v_rcp_f32_e32 v182, v182
	v_mul_f32_e32 v162, v79, v162
	v_mul_f32_e32 v181, 0x3c000000, v162
	v_mul_f32_e32 v162, v80, v163
	v_add_f32_e32 v163, 1.0, v161
	v_rcp_f32_e32 v163, v163
	v_mul_f32_e32 v183, 0x3c000000, v162
	v_add_f32_e32 v5, 1.0, v158
	v_rcp_f32_e32 v5, v5
	v_mul_f32_e32 v162, v81, v163
	v_add_f32_e32 v163, 1.0, v9
	v_mul_f32_e32 v184, 0x3c000000, v162
	v_mul_f32_e32 v162, v74, v182
	v_rcp_f32_e32 v163, v163
	v_add_f32_e32 v182, 1.0, v156
	v_rcp_f32_e32 v182, v182
	v_mul_f32_e32 v185, 0x3c000000, v162
	v_mul_f32_e32 v162, v75, v163
	v_mul_f32_e32 v186, 0x3c000000, v162
	v_mul_f32_e32 v162, v76, v182
	v_mul_f32_e32 v182, 0x3c000000, v162
	v_add_f32_e32 v162, 1.0, v157
	v_mul_f32_e32 v5, v78, v5
	v_rcp_f32_e32 v187, v162
	v_mul_f32_e32 v5, 0x3c000000, v5
	v_mov_b32_e32 v162, 0
	v_mov_b32_e32 v163, 0
	v_cvt_pk_fp8_f32 v162, v5, v181
	v_cvt_pk_fp8_f32 v163, v185, v186
	v_mul_f32_e32 v5, v77, v187
	v_mul_f32_e32 v5, 0x3c000000, v5
	v_cvt_pk_fp8_f32 v162, v183, v184 op_sel:[0,0,1]
	v_cvt_pk_fp8_f32 v163, v182, v5 op_sel:[0,0,1]
	ds_write_b64 v180, v[162:163] offset:32
	s_cbranch_execz .LBB0_631

; #define LAS __attribute__((address_space(3)))
; __device__ __forceinline__ unsigned pk4_fp8(float a, float b, float c, float d) { int w = 0; w = __builtin_amdgcn_cvt_pk_fp8_f32(a, b, w, false); w = __builtin_amdgcn_cvt_pk_fp8_f32(c, d, w, true); return (unsigned)w; }
; __device__ __forceinline__ float bf_lo(unsigned w) { return __uint_as_float(w << 16); }
; __device__ __forceinline__ float bf_hi(unsigned w) { return __uint_as_float(w & 0xffff0000u); }
; __device__ __forceinline__ float sigmoidf_fast(float x) { return __builtin_amdgcn_rcpf(1.0f + __builtin_amdgcn_exp2f(-1.4426950408889634f * x)); }
;     __device__ __forceinline__ void operator()(f32x4 (&acc)[2][2][4][2], const Unit& u, int wr, int wc, int fr, int fq) const {
;     ...
;                 const size_t ro = (size_t)(u.row0 + ai * 128 + wr * 64 + m * 16 + fr) * DM + col0;
; #pragma unroll
;                 for (int bj = 0; bj < 2; ++bj) {
;                     const u32x4 gd = *(const u32x4*)(GDF + ro + bj * 32);
;                     const float ed[8] = {bf_lo(gd.x), bf_hi(gd.x), bf_lo(gd.y), bf_hi(gd.y), bf_lo(gd.z), bf_hi(gd.z), bf_lo(gd.w), bf_hi(gd.w)};
;                     if (u.tag == 0) {
;                         const u32x4 gn = *(const u32x4*)(GNA + ro + bj * 32);
;                         const float en[8] = {bf_lo(gn.x), bf_hi(gn.x), bf_lo(gn.y), bf_hi(gn.y), bf_lo(gn.z), bf_hi(gn.z), bf_lo(gn.w), bf_hi(gn.w)};
; #pragma unroll
;                         for (int e = 0; e < 8; ++e) {
;                             const float r = (1.0f + __builtin_amdgcn_exp2f(-1.4426950408889634f * ed[e])) * __builtin_amdgcn_rcpf(1.0f + __builtin_amdgcn_exp2f(-1.4426950408889634f * en[e]));
;                             acc[ai][bj][m][e >> 2][e & 3] *= r; }
;                     } else {
;                         float y[8];
; #pragma unroll
;                         for (int e = 0; e < 8; ++e) y[e] = acc[ai][bj][m][e >> 2][e & 3] * sigmoidf_fast(ed[e]) * (PSCALE * WSCALE_INV * OSCALE_INV);
;                         u32x2 w; w.x = pk4_fp8(y[0], y[1], y[2], y[3]); w.y = pk4_fp8(y[4], y[5], y[6], y[7]);
;                         *(LAS u32x2*)(my + fr * 80 + bj * 32 + fq * 8) = w;
;                     }
.LBB0_593:
	s_nop 1
	v_add_u32_e32 v6, 0x80, v4
	v_ashrrev_i32_e32 v7, 31, v6
	v_lshlrev_b64 v[6:7], 11, v[6:7]
	v_lshl_add_u64 v[6:7], v[6:7], 0, v[2:3]
	v_lshl_add_u64 v[8:9], v[6:7], 1, s[40:41]
	global_load_dwordx4 v[156:159], v[8:9], off nt
	s_and_b64 vcc, exec, s[4:5]
	s_mov_b64 s[58:59], -1
	s_waitcnt vmcnt(0)
	v_lshlrev_b32_e32 v5, 16, v156
	v_and_b32_e32 v156, 0xffff0000, v156
	v_lshlrev_b32_e32 v160, 16, v157
	v_and_b32_e32 v157, 0xffff0000, v157
	v_lshlrev_b32_e32 v161, 16, v158
	v_and_b32_e32 v158, 0xffff0000, v158
	v_lshlrev_b32_e32 v162, 16, v159
	v_and_b32_e32 v159, 0xffff0000, v159
	v_mul_f32_e32 v5, 0xbfb8aa3b, v5
	v_mul_f32_e32 v156, 0xbfb8aa3b, v156
	v_mul_f32_e32 v163, 0xbfb8aa3b, v160
	v_mul_f32_e32 v157, 0xbfb8aa3b, v157
	v_mul_f32_e32 v181, 0xbfb8aa3b, v161
	v_mul_f32_e32 v158, 0xbfb8aa3b, v158
	v_mul_f32_e32 v182, 0xbfb8aa3b, v162
	v_mul_f32_e32 v159, 0xbfb8aa3b, v159
	v_exp_f32_e32 v160, v5
	v_exp_f32_e32 v161, v156
	v_exp_f32_e32 v162, v163
	v_exp_f32_e32 v163, v157
	v_exp_f32_e32 v156, v181
	v_exp_f32_e32 v157, v158
	v_exp_f32_e32 v158, v182
	v_exp_f32_e32 v159, v159
	s_cbranch_vccnz .LBB0_595
	v_add_f32_e32 v182, 1.0, v162
	v_rcp_f32_e32 v182, v182
	v_add_f32_e32 v183, 1.0, v163
	v_rcp_f32_e32 v183, v183
	v_add_f32_e32 v184, 1.0, v156
	v_rcp_f32_e32 v184, v184
	v_mul_f32_e32 v182, v72, v182
	v_mul_f32_e32 v185, 0x3c000000, v182
	v_mul_f32_e32 v182, v73, v183
	v_add_f32_e32 v183, 1.0, v157
	v_mul_f32_e32 v186, 0x3c000000, v182
	v_mul_f32_e32 v182, v66, v184
	v_rcp_f32_e32 v183, v183
	v_add_f32_e32 v184, 1.0, v158
	v_rcp_f32_e32 v184, v184
	v_add_f32_e32 v5, 1.0, v160
	v_add_f32_e32 v181, 1.0, v161
	v_rcp_f32_e32 v5, v5
	v_rcp_f32_e32 v181, v181
	v_mul_f32_e32 v187, 0x3c000000, v182
	v_mul_f32_e32 v182, v67, v183
	v_mul_f32_e32 v188, 0x3c000000, v182
	v_mul_f32_e32 v182, v68, v184
	v_mul_f32_e32 v184, 0x3c000000, v182
	v_add_f32_e32 v182, 1.0, v159
	v_mul_f32_e32 v5, v70, v5
	v_mul_f32_e32 v181, v71, v181
	v_rcp_f32_e32 v189, v182
	v_mul_f32_e32 v5, 0x3c000000, v5
	v_mul_f32_e32 v181, 0x3c000000, v181
	v_mov_b32_e32 v182, 0
	v_mov_b32_e32 v183, 0
	v_cvt_pk_fp8_f32 v182, v5, v181
	v_cvt_pk_fp8_f32 v183, v187, v188
	v_mul_f32_e32 v5, v69, v189
	v_mul_f32_e32 v5, 0x3c000000, v5
	v_cvt_pk_fp8_f32 v182, v185, v186 op_sel:[0,0,1]
	v_cvt_pk_fp8_f32 v183, v184, v5 op_sel:[0,0,1]
	s_mov_b64 s[58:59], 0
	ds_write_b64 v180, v[182:183]
.LBB0_595:
	s_andn2_b64 vcc, exec, s[58:59]
	v_lshl_add_u64 v[6:7], v[6:7], 1, s[38:39]
	s_cbranch_vccnz .LBB0_597
	global_load_dwordx4 v[182:185], v[6:7], off nt
	v_pk_add_f32 v[162:163], v[162:163], 1.0 op_sel_hi:[1,0]
	v_pk_add_f32 v[160:161], v[160:161], 1.0 op_sel_hi:[1,0]
	v_pk_add_f32 v[158:159], v[158:159], 1.0 op_sel_hi:[1,0]
	v_pk_add_f32 v[156:157], v[156:157], 1.0 op_sel_hi:[1,0]
	s_waitcnt vmcnt(0)
	v_lshlrev_b32_e32 v5, 16, v182
	v_and_b32_e32 v181, 0xffff0000, v182
	v_lshlrev_b32_e32 v182, 16, v183
	v_and_b32_e32 v183, 0xffff0000, v183
	v_lshlrev_b32_e32 v186, 16, v184
	v_and_b32_e32 v184, 0xffff0000, v184
	v_lshlrev_b32_e32 v187, 16, v185
	v_and_b32_e32 v185, 0xffff0000, v185
	v_mul_f32_e32 v5, 0xbfb8aa3b, v5
	v_mul_f32_e32 v181, 0xbfb8aa3b, v181
	v_mul_f32_e32 v182, 0xbfb8aa3b, v182
	v_mul_f32_e32 v183, 0xbfb8aa3b, v183
	v_mul_f32_e32 v186, 0xbfb8aa3b, v186
	v_mul_f32_e32 v184, 0xbfb8aa3b, v184
	v_mul_f32_e32 v187, 0xbfb8aa3b, v187
	v_mul_f32_e32 v185, 0xbfb8aa3b, v185
	v_exp_f32_e32 v5, v5
	v_exp_f32_e32 v181, v181
	v_exp_f32_e32 v182, v182
	v_exp_f32_e32 v183, v183
	v_exp_f32_e32 v186, v186
	v_exp_f32_e32 v184, v184
	v_exp_f32_e32 v187, v187
	v_exp_f32_e32 v185, v185
	v_add_f32_e32 v5, 1.0, v5
	v_add_f32_e32 v181, 1.0, v181
	v_add_f32_e32 v188, 1.0, v182
	v_add_f32_e32 v189, 1.0, v183
	v_add_f32_e32 v186, 1.0, v186
	v_add_f32_e32 v190, 1.0, v184
	v_add_f32_e32 v191, 1.0, v187
	v_add_f32_e32 v192, 1.0, v185
	v_rcp_f32_e32 v182, v5
	v_rcp_f32_e32 v183, v181
	v_rcp_f32_e32 v184, v188
	v_rcp_f32_e32 v185, v189
	v_rcp_f32_e32 v186, v186
	v_rcp_f32_e32 v187, v190
	v_rcp_f32_e32 v188, v191
	v_rcp_f32_e32 v189, v192
	v_pk_mul_f32 v[160:161], v[160:161], v[182:183]
	v_pk_mul_f32 v[162:163], v[162:163], v[184:185]
	v_pk_mul_f32 v[156:157], v[156:157], v[186:187]
	v_pk_mul_f32 v[158:159], v[158:159], v[188:189]
	v_pk_mul_f32 v[72:73], v[72:73], v[162:163]
	v_pk_mul_f32 v[70:71], v[70:71], v[160:161]
	v_pk_mul_f32 v[68:69], v[68:69], v[158:159]
	v_pk_mul_f32 v[66:67], v[66:67], v[156:157]
.LBB0_597:
	global_load_dwordx4 v[156:159], v[8:9], off offset:64 nt
	s_and_b64 vcc, exec, s[4:5]
	s_mov_b64 s[58:59], -1
	s_waitcnt vmcnt(0)
	v_lshlrev_b32_e32 v5, 16, v156
	v_and_b32_e32 v8, 0xffff0000, v156
	v_lshlrev_b32_e32 v9, 16, v157
	v_and_b32_e32 v156, 0xffff0000, v157
	v_lshlrev_b32_e32 v157, 16, v158
	v_and_b32_e32 v158, 0xffff0000, v158
	v_lshlrev_b32_e32 v160, 16, v159
	v_and_b32_e32 v159, 0xffff0000, v159
	v_mul_f32_e32 v5, 0xbfb8aa3b, v5
	v_mul_f32_e32 v8, 0xbfb8aa3b, v8
	v_mul_f32_e32 v9, 0xbfb8aa3b, v9
	v_mul_f32_e32 v156, 0xbfb8aa3b, v156
	v_mul_f32_e32 v157, 0xbfb8aa3b, v157
	v_mul_f32_e32 v162, 0xbfb8aa3b, v158
	v_mul_f32_e32 v163, 0xbfb8aa3b, v160
	v_mul_f32_e32 v181, 0xbfb8aa3b, v159
	v_exp_f32_e32 v158, v5
	v_exp_f32_e32 v159, v8
	v_exp_f32_e32 v160, v9
	v_exp_f32_e32 v161, v156
	v_exp_f32_e32 v8, v157
	v_exp_f32_e32 v9, v162
	v_exp_f32_e32 v156, v163
	v_exp_f32_e32 v157, v181
	s_cbranch_vccnz .LBB0_632
	v_add_f32_e32 v162, 1.0, v159
	v_add_f32_e32 v163, 1.0, v160
	v_rcp_f32_e32 v162, v162
	v_rcp_f32_e32 v163, v163
	v_add_f32_e32 v182, 1.0, v8
	v_rcp_f32_e32 v182, v182
	v_mul_f32_e32 v162, v39, v162
	v_mul_f32_e32 v181, 0x3c000000, v162
	v_mul_f32_e32 v162, v40, v163
	v_add_f32_e32 v163, 1.0, v161
	v_rcp_f32_e32 v163, v163
	v_mul_f32_e32 v183, 0x3c000000, v162
	v_add_f32_e32 v5, 1.0, v158
	v_rcp_f32_e32 v5, v5
	v_mul_f32_e32 v162, v41, v163
	v_add_f32_e32 v163, 1.0, v9
	v_mul_f32_e32 v184, 0x3c000000, v162
	v_mul_f32_e32 v162, v34, v182
	v_rcp_f32_e32 v163, v163
	v_add_f32_e32 v182, 1.0, v156
	v_rcp_f32_e32 v182, v182
	v_mul_f32_e32 v185, 0x3c000000, v162
	v_mul_f32_e32 v162, v35, v163
	v_mul_f32_e32 v186, 0x3c000000, v162
	v_mul_f32_e32 v162, v36, v182
	v_mul_f32_e32 v182, 0x3c000000, v162
	v_add_f32_e32 v162, 1.0, v157
	v_mul_f32_e32 v5, v38, v5
	v_rcp_f32_e32 v187, v162
	v_mul_f32_e32 v5, 0x3c000000, v5
	v_mov_b32_e32 v162, 0
	v_mov_b32_e32 v163, 0
	v_cvt_pk_fp8_f32 v162, v5, v181
	v_cvt_pk_fp8_f32 v163, v185, v186
	v_mul_f32_e32 v5, v37, v187
	v_mul_f32_e32 v5, 0x3c000000, v5
	v_cvt_pk_fp8_f32 v162, v183, v184 op_sel:[0,0,1]
	v_cvt_pk_fp8_f32 v163, v182, v5 op_sel:[0,0,1]
	ds_write_b64 v180, v[162:163] offset:32
	s_cbranch_execz .LBB0_633

; #define LAS __attribute__((address_space(3)))
; __device__ __forceinline__ unsigned pk4_fp8(float a, float b, float c, float d) { int w = 0; w = __builtin_amdgcn_cvt_pk_fp8_f32(a, b, w, false); w = __builtin_amdgcn_cvt_pk_fp8_f32(c, d, w, true); return (unsigned)w; }
; __device__ __forceinline__ float bf_lo(unsigned w) { return __uint_as_float(w << 16); }
; __device__ __forceinline__ float bf_hi(unsigned w) { return __uint_as_float(w & 0xffff0000u); }
; __device__ __forceinline__ float sigmoidf_fast(float x) { return __builtin_amdgcn_rcpf(1.0f + __builtin_amdgcn_exp2f(-1.4426950408889634f * x)); }
;     __device__ __forceinline__ void operator()(f32x4 (&acc)[2][2][4][2], const Unit& u, int wr, int wc, int fr, int fq) const {
;     ...
;                 const size_t ro = (size_t)(u.row0 + ai * 128 + wr * 64 + m * 16 + fr) * DM + col0;
; #pragma unroll
;                 for (int bj = 0; bj < 2; ++bj) {
;                     const u32x4 gd = *(const u32x4*)(GDF + ro + bj * 32);
;                     const float ed[8] = {bf_lo(gd.x), bf_hi(gd.x), bf_lo(gd.y), bf_hi(gd.y), bf_lo(gd.z), bf_hi(gd.z), bf_lo(gd.w), bf_hi(gd.w)};
;                     if (u.tag == 0) {
;                         const u32x4 gn = *(const u32x4*)(GNA + ro + bj * 32);
;                         const float en[8] = {bf_lo(gn.x), bf_hi(gn.x), bf_lo(gn.y), bf_hi(gn.y), bf_lo(gn.z), bf_hi(gn.z), bf_lo(gn.w), bf_hi(gn.w)};
; #pragma unroll
;                         for (int e = 0; e < 8; ++e) {
;                             const float r = (1.0f + __builtin_amdgcn_exp2f(-1.4426950408889634f * ed[e])) * __builtin_amdgcn_rcpf(1.0f + __builtin_amdgcn_exp2f(-1.4426950408889634f * en[e]));
;                             acc[ai][bj][m][e >> 2][e & 3] *= r; }
;                     } else {
;                         float y[8];
; #pragma unroll
;                         for (int e = 0; e < 8; ++e) y[e] = acc[ai][bj][m][e >> 2][e & 3] * sigmoidf_fast(ed[e]) * (PSCALE * WSCALE_INV * OSCALE_INV);
;                         u32x2 w; w.x = pk4_fp8(y[0], y[1], y[2], y[3]); w.y = pk4_fp8(y[4], y[5], y[6], y[7]);
;                         *(LAS u32x2*)(my + fr * 80 + bj * 32 + fq * 8) = w;
;                     }
.LBB0_601:
	s_nop 1
	v_add_u32_e32 v6, 0x90, v4
	v_ashrrev_i32_e32 v7, 31, v6
	v_lshlrev_b64 v[6:7], 11, v[6:7]
	v_lshl_add_u64 v[6:7], v[6:7], 0, v[2:3]
	v_lshl_add_u64 v[8:9], v[6:7], 1, s[40:41]
	global_load_dwordx4 v[156:159], v[8:9], off nt
	s_and_b64 vcc, exec, s[4:5]
	s_mov_b64 s[58:59], -1
	s_waitcnt vmcnt(0)
	v_lshlrev_b32_e32 v5, 16, v156
	v_and_b32_e32 v156, 0xffff0000, v156
	v_lshlrev_b32_e32 v160, 16, v157
	v_and_b32_e32 v157, 0xffff0000, v157
	v_lshlrev_b32_e32 v161, 16, v158
	v_and_b32_e32 v158, 0xffff0000, v158
	v_lshlrev_b32_e32 v162, 16, v159
	v_and_b32_e32 v159, 0xffff0000, v159
	v_mul_f32_e32 v5, 0xbfb8aa3b, v5
	v_mul_f32_e32 v156, 0xbfb8aa3b, v156
	v_mul_f32_e32 v163, 0xbfb8aa3b, v160
	v_mul_f32_e32 v157, 0xbfb8aa3b, v157
	v_mul_f32_e32 v181, 0xbfb8aa3b, v161
	v_mul_f32_e32 v158, 0xbfb8aa3b, v158
	v_mul_f32_e32 v182, 0xbfb8aa3b, v162
	v_mul_f32_e32 v159, 0xbfb8aa3b, v159
	v_exp_f32_e32 v160, v5
	v_exp_f32_e32 v161, v156
	v_exp_f32_e32 v162, v163
	v_exp_f32_e32 v163, v157
	v_exp_f32_e32 v156, v181
	v_exp_f32_e32 v157, v158
	v_exp_f32_e32 v158, v182
	v_exp_f32_e32 v159, v159
	s_cbranch_vccnz .LBB0_603
	v_add_f32_e32 v182, 1.0, v162
	v_rcp_f32_e32 v182, v182
	v_add_f32_e32 v183, 1.0, v163
	v_rcp_f32_e32 v183, v183
	v_add_f32_e32 v184, 1.0, v156
	v_rcp_f32_e32 v184, v184
	v_mul_f32_e32 v182, v64, v182
	v_mul_f32_e32 v185, 0x3c000000, v182
	v_mul_f32_e32 v182, v65, v183
	v_add_f32_e32 v183, 1.0, v157
	v_mul_f32_e32 v186, 0x3c000000, v182
	v_mul_f32_e32 v182, v58, v184
	v_rcp_f32_e32 v183, v183
	v_add_f32_e32 v184, 1.0, v158
	v_rcp_f32_e32 v184, v184
	v_add_f32_e32 v5, 1.0, v160
	v_add_f32_e32 v181, 1.0, v161
	v_rcp_f32_e32 v5, v5
	v_rcp_f32_e32 v181, v181
	v_mul_f32_e32 v187, 0x3c000000, v182
	v_mul_f32_e32 v182, v59, v183
	v_mul_f32_e32 v188, 0x3c000000, v182
	v_mul_f32_e32 v182, v60, v184
	v_mul_f32_e32 v184, 0x3c000000, v182
	v_add_f32_e32 v182, 1.0, v159
	v_mul_f32_e32 v5, v62, v5
	v_mul_f32_e32 v181, v63, v181
	v_rcp_f32_e32 v189, v182
	v_mul_f32_e32 v5, 0x3c000000, v5
	v_mul_f32_e32 v181, 0x3c000000, v181
	v_mov_b32_e32 v182, 0
	v_mov_b32_e32 v183, 0
	v_cvt_pk_fp8_f32 v182, v5, v181
	v_cvt_pk_fp8_f32 v183, v187, v188
	v_mul_f32_e32 v5, v61, v189
	v_mul_f32_e32 v5, 0x3c000000, v5
	v_cvt_pk_fp8_f32 v182, v185, v186 op_sel:[0,0,1]
	v_cvt_pk_fp8_f32 v183, v184, v5 op_sel:[0,0,1]
	s_mov_b64 s[58:59], 0
	ds_write_b64 v180, v[182:183]
.LBB0_603:
	s_andn2_b64 vcc, exec, s[58:59]
	v_lshl_add_u64 v[6:7], v[6:7], 1, s[38:39]
	s_cbranch_vccnz .LBB0_605
	global_load_dwordx4 v[182:185], v[6:7], off nt
	v_pk_add_f32 v[162:163], v[162:163], 1.0 op_sel_hi:[1,0]
	v_pk_add_f32 v[160:161], v[160:161], 1.0 op_sel_hi:[1,0]
	v_pk_add_f32 v[158:159], v[158:159], 1.0 op_sel_hi:[1,0]
	v_pk_add_f32 v[156:157], v[156:157], 1.0 op_sel_hi:[1,0]
	s_waitcnt vmcnt(0)
	v_lshlrev_b32_e32 v5, 16, v182
	v_and_b32_e32 v181, 0xffff0000, v182
	v_lshlrev_b32_e32 v182, 16, v183
	v_and_b32_e32 v183, 0xffff0000, v183
	v_lshlrev_b32_e32 v186, 16, v184
	v_and_b32_e32 v184, 0xffff0000, v184
	v_lshlrev_b32_e32 v187, 16, v185
	v_and_b32_e32 v185, 0xffff0000, v185
	v_mul_f32_e32 v5, 0xbfb8aa3b, v5
	v_mul_f32_e32 v181, 0xbfb8aa3b, v181
	v_mul_f32_e32 v182, 0xbfb8aa3b, v182
	v_mul_f32_e32 v183, 0xbfb8aa3b, v183
	v_mul_f32_e32 v186, 0xbfb8aa3b, v186
	v_mul_f32_e32 v184, 0xbfb8aa3b, v184
	v_mul_f32_e32 v187, 0xbfb8aa3b, v187
	v_mul_f32_e32 v185, 0xbfb8aa3b, v185
	v_exp_f32_e32 v5, v5
	v_exp_f32_e32 v181, v181
	v_exp_f32_e32 v182, v182
	v_exp_f32_e32 v183, v183
	v_exp_f32_e32 v186, v186
	v_exp_f32_e32 v184, v184
	v_exp_f32_e32 v187, v187
	v_exp_f32_e32 v185, v185
	v_add_f32_e32 v5, 1.0, v5
	v_add_f32_e32 v181, 1.0, v181
	v_add_f32_e32 v188, 1.0, v182
	v_add_f32_e32 v189, 1.0, v183
	v_add_f32_e32 v186, 1.0, v186
	v_add_f32_e32 v190, 1.0, v184
	v_add_f32_e32 v191, 1.0, v187
	v_add_f32_e32 v192, 1.0, v185
	v_rcp_f32_e32 v182, v5
	v_rcp_f32_e32 v183, v181
	v_rcp_f32_e32 v184, v188
	v_rcp_f32_e32 v185, v189
	v_rcp_f32_e32 v186, v186
	v_rcp_f32_e32 v187, v190
	v_rcp_f32_e32 v188, v191
	v_rcp_f32_e32 v189, v192
	v_pk_mul_f32 v[160:161], v[160:161], v[182:183]
	v_pk_mul_f32 v[162:163], v[162:163], v[184:185]
	v_pk_mul_f32 v[156:157], v[156:157], v[186:187]
	v_pk_mul_f32 v[158:159], v[158:159], v[188:189]
	v_pk_mul_f32 v[64:65], v[64:65], v[162:163]
	v_pk_mul_f32 v[62:63], v[62:63], v[160:161]
	v_pk_mul_f32 v[60:61], v[60:61], v[158:159]
	v_pk_mul_f32 v[58:59], v[58:59], v[156:157]
.LBB0_605:
	global_load_dwordx4 v[156:159], v[8:9], off offset:64 nt
	s_and_b64 vcc, exec, s[4:5]
	s_mov_b64 s[58:59], -1
	s_waitcnt vmcnt(0)
	v_lshlrev_b32_e32 v5, 16, v156
	v_and_b32_e32 v8, 0xffff0000, v156
	v_lshlrev_b32_e32 v9, 16, v157
	v_and_b32_e32 v156, 0xffff0000, v157
	v_lshlrev_b32_e32 v157, 16, v158
	v_and_b32_e32 v158, 0xffff0000, v158
	v_lshlrev_b32_e32 v160, 16, v159
	v_and_b32_e32 v159, 0xffff0000, v159
	v_mul_f32_e32 v5, 0xbfb8aa3b, v5
	v_mul_f32_e32 v8, 0xbfb8aa3b, v8
	v_mul_f32_e32 v9, 0xbfb8aa3b, v9
	v_mul_f32_e32 v156, 0xbfb8aa3b, v156
	v_mul_f32_e32 v157, 0xbfb8aa3b, v157
	v_mul_f32_e32 v162, 0xbfb8aa3b, v158
	v_mul_f32_e32 v163, 0xbfb8aa3b, v160
	v_mul_f32_e32 v181, 0xbfb8aa3b, v159
	v_exp_f32_e32 v158, v5
	v_exp_f32_e32 v159, v8
	v_exp_f32_e32 v160, v9
	v_exp_f32_e32 v161, v156
	v_exp_f32_e32 v8, v157
	v_exp_f32_e32 v9, v162
	v_exp_f32_e32 v156, v163
	v_exp_f32_e32 v157, v181
	s_cbranch_vccnz .LBB0_634
	v_add_f32_e32 v162, 1.0, v159
	v_add_f32_e32 v163, 1.0, v160
	v_rcp_f32_e32 v162, v162
	v_rcp_f32_e32 v163, v163
	v_add_f32_e32 v182, 1.0, v8
	v_rcp_f32_e32 v182, v182
	v_mul_f32_e32 v162, v31, v162
	v_mul_f32_e32 v181, 0x3c000000, v162
	v_mul_f32_e32 v162, v32, v163
	v_add_f32_e32 v163, 1.0, v161
	v_rcp_f32_e32 v163, v163
	v_mul_f32_e32 v183, 0x3c000000, v162
	v_add_f32_e32 v5, 1.0, v158
	v_rcp_f32_e32 v5, v5
	v_mul_f32_e32 v162, v33, v163
	v_add_f32_e32 v163, 1.0, v9
	v_mul_f32_e32 v184, 0x3c000000, v162
	v_mul_f32_e32 v162, v26, v182
	v_rcp_f32_e32 v163, v163
	v_add_f32_e32 v182, 1.0, v156
	v_rcp_f32_e32 v182, v182
	v_mul_f32_e32 v185, 0x3c000000, v162
	v_mul_f32_e32 v162, v27, v163
	v_mul_f32_e32 v186, 0x3c000000, v162
	v_mul_f32_e32 v162, v28, v182
	v_mul_f32_e32 v182, 0x3c000000, v162
	v_add_f32_e32 v162, 1.0, v157
	v_mul_f32_e32 v5, v30, v5
	v_rcp_f32_e32 v187, v162
	v_mul_f32_e32 v5, 0x3c000000, v5
	v_mov_b32_e32 v162, 0
	v_mov_b32_e32 v163, 0
	v_cvt_pk_fp8_f32 v162, v5, v181
	v_cvt_pk_fp8_f32 v163, v185, v186
	v_mul_f32_e32 v5, v29, v187
	v_mul_f32_e32 v5, 0x3c000000, v5
	v_cvt_pk_fp8_f32 v162, v183, v184 op_sel:[0,0,1]
	v_cvt_pk_fp8_f32 v163, v182, v5 op_sel:[0,0,1]
	ds_write_b64 v180, v[162:163] offset:32
	s_cbranch_execz .LBB0_635

; #define LAS __attribute__((address_space(3)))
; __device__ __forceinline__ unsigned pk4_fp8(float a, float b, float c, float d) { int w = 0; w = __builtin_amdgcn_cvt_pk_fp8_f32(a, b, w, false); w = __builtin_amdgcn_cvt_pk_fp8_f32(c, d, w, true); return (unsigned)w; }
; __device__ __forceinline__ float bf_lo(unsigned w) { return __uint_as_float(w << 16); }
; __device__ __forceinline__ float bf_hi(unsigned w) { return __uint_as_float(w & 0xffff0000u); }
; __device__ __forceinline__ float sigmoidf_fast(float x) { return __builtin_amdgcn_rcpf(1.0f + __builtin_amdgcn_exp2f(-1.4426950408889634f * x)); }
;     __device__ __forceinline__ void operator()(f32x4 (&acc)[2][2][4][2], const Unit& u, int wr, int wc, int fr, int fq) const {
;     ...
;                 const size_t ro = (size_t)(u.row0 + ai * 128 + wr * 64 + m * 16 + fr) * DM + col0;
; #pragma unroll
;                 for (int bj = 0; bj < 2; ++bj) {
;                     const u32x4 gd = *(const u32x4*)(GDF + ro + bj * 32);
;                     const float ed[8] = {bf_lo(gd.x), bf_hi(gd.x), bf_lo(gd.y), bf_hi(gd.y), bf_lo(gd.z), bf_hi(gd.z), bf_lo(gd.w), bf_hi(gd.w)};
;                     if (u.tag == 0) {
;                         const u32x4 gn = *(const u32x4*)(GNA + ro + bj * 32);
;                         const float en[8] = {bf_lo(gn.x), bf_hi(gn.x), bf_lo(gn.y), bf_hi(gn.y), bf_lo(gn.z), bf_hi(gn.z), bf_lo(gn.w), bf_hi(gn.w)};
; #pragma unroll
;                         for (int e = 0; e < 8; ++e) {
;                             const float r = (1.0f + __builtin_amdgcn_exp2f(-1.4426950408889634f * ed[e])) * __builtin_amdgcn_rcpf(1.0f + __builtin_amdgcn_exp2f(-1.4426950408889634f * en[e]));
;                             acc[ai][bj][m][e >> 2][e & 3] *= r; }
;                     } else {
;                         float y[8];
; #pragma unroll
;                         for (int e = 0; e < 8; ++e) y[e] = acc[ai][bj][m][e >> 2][e & 3] * sigmoidf_fast(ed[e]) * (PSCALE * WSCALE_INV * OSCALE_INV);
;                         u32x2 w; w.x = pk4_fp8(y[0], y[1], y[2], y[3]); w.y = pk4_fp8(y[4], y[5], y[6], y[7]);
;                         *(LAS u32x2*)(my + fr * 80 + bj * 32 + fq * 8) = w;
;                     }
.LBB0_609:
	s_nop 1
	v_add_u32_e32 v6, 0xa0, v4
	v_ashrrev_i32_e32 v7, 31, v6
	v_lshlrev_b64 v[6:7], 11, v[6:7]
	v_lshl_add_u64 v[6:7], v[6:7], 0, v[2:3]
	v_lshl_add_u64 v[8:9], v[6:7], 1, s[40:41]
	global_load_dwordx4 v[156:159], v[8:9], off nt
	s_and_b64 vcc, exec, s[4:5]
	s_mov_b64 s[58:59], -1
	s_waitcnt vmcnt(0)
	v_lshlrev_b32_e32 v5, 16, v156
	v_and_b32_e32 v156, 0xffff0000, v156
	v_lshlrev_b32_e32 v160, 16, v157
	v_and_b32_e32 v157, 0xffff0000, v157
	v_lshlrev_b32_e32 v161, 16, v158
	v_and_b32_e32 v158, 0xffff0000, v158
	v_lshlrev_b32_e32 v162, 16, v159
	v_and_b32_e32 v159, 0xffff0000, v159
	v_mul_f32_e32 v5, 0xbfb8aa3b, v5
	v_mul_f32_e32 v156, 0xbfb8aa3b, v156
	v_mul_f32_e32 v163, 0xbfb8aa3b, v160
	v_mul_f32_e32 v157, 0xbfb8aa3b, v157
	v_mul_f32_e32 v181, 0xbfb8aa3b, v161
	v_mul_f32_e32 v158, 0xbfb8aa3b, v158
	v_mul_f32_e32 v182, 0xbfb8aa3b, v162
	v_mul_f32_e32 v159, 0xbfb8aa3b, v159
	v_exp_f32_e32 v160, v5
	v_exp_f32_e32 v161, v156
	v_exp_f32_e32 v162, v163
	v_exp_f32_e32 v163, v157
	v_exp_f32_e32 v156, v181
	v_exp_f32_e32 v157, v158
	v_exp_f32_e32 v158, v182
	v_exp_f32_e32 v159, v159
	s_cbranch_vccnz .LBB0_611
	v_add_f32_e32 v182, 1.0, v162
	v_rcp_f32_e32 v182, v182
	v_add_f32_e32 v183, 1.0, v163
	v_rcp_f32_e32 v183, v183
	v_add_f32_e32 v184, 1.0, v156
	v_rcp_f32_e32 v184, v184
	v_mul_f32_e32 v182, v56, v182
	v_mul_f32_e32 v185, 0x3c000000, v182
	v_mul_f32_e32 v182, v57, v183
	v_add_f32_e32 v183, 1.0, v157
	v_mul_f32_e32 v186, 0x3c000000, v182
	v_mul_f32_e32 v182, v50, v184
	v_rcp_f32_e32 v183, v183
	v_add_f32_e32 v184, 1.0, v158
	v_rcp_f32_e32 v184, v184
	v_add_f32_e32 v5, 1.0, v160
	v_add_f32_e32 v181, 1.0, v161
	v_rcp_f32_e32 v5, v5
	v_rcp_f32_e32 v181, v181
	v_mul_f32_e32 v187, 0x3c000000, v182
	v_mul_f32_e32 v182, v51, v183
	v_mul_f32_e32 v188, 0x3c000000, v182
	v_mul_f32_e32 v182, v52, v184
	v_mul_f32_e32 v184, 0x3c000000, v182
	v_add_f32_e32 v182, 1.0, v159
	v_mul_f32_e32 v5, v54, v5
	v_mul_f32_e32 v181, v55, v181
	v_rcp_f32_e32 v189, v182
	v_mul_f32_e32 v5, 0x3c000000, v5
	v_mul_f32_e32 v181, 0x3c000000, v181
	v_mov_b32_e32 v182, 0
	v_mov_b32_e32 v183, 0
	v_cvt_pk_fp8_f32 v182, v5, v181
	v_cvt_pk_fp8_f32 v183, v187, v188
	v_mul_f32_e32 v5, v53, v189
	v_mul_f32_e32 v5, 0x3c000000, v5
	v_cvt_pk_fp8_f32 v182, v185, v186 op_sel:[0,0,1]
	v_cvt_pk_fp8_f32 v183, v184, v5 op_sel:[0,0,1]
	s_mov_b64 s[58:59], 0
	ds_write_b64 v180, v[182:183]
.LBB0_611:
	s_andn2_b64 vcc, exec, s[58:59]
	v_lshl_add_u64 v[6:7], v[6:7], 1, s[38:39]
	s_cbranch_vccnz .LBB0_613
	global_load_dwordx4 v[182:185], v[6:7], off nt
	v_pk_add_f32 v[162:163], v[162:163], 1.0 op_sel_hi:[1,0]
	v_pk_add_f32 v[160:161], v[160:161], 1.0 op_sel_hi:[1,0]
	v_pk_add_f32 v[158:159], v[158:159], 1.0 op_sel_hi:[1,0]
	v_pk_add_f32 v[156:157], v[156:157], 1.0 op_sel_hi:[1,0]
	s_waitcnt vmcnt(0)
	v_lshlrev_b32_e32 v5, 16, v182
	v_and_b32_e32 v181, 0xffff0000, v182
	v_lshlrev_b32_e32 v182, 16, v183
	v_and_b32_e32 v183, 0xffff0000, v183
	v_lshlrev_b32_e32 v186, 16, v184
	v_and_b32_e32 v184, 0xffff0000, v184
	v_lshlrev_b32_e32 v187, 16, v185
	v_and_b32_e32 v185, 0xffff0000, v185
	v_mul_f32_e32 v5, 0xbfb8aa3b, v5
	v_mul_f32_e32 v181, 0xbfb8aa3b, v181
	v_mul_f32_e32 v182, 0xbfb8aa3b, v182
	v_mul_f32_e32 v183, 0xbfb8aa3b, v183
	v_mul_f32_e32 v186, 0xbfb8aa3b, v186
	v_mul_f32_e32 v184, 0xbfb8aa3b, v184
	v_mul_f32_e32 v187, 0xbfb8aa3b, v187
	v_mul_f32_e32 v185, 0xbfb8aa3b, v185
	v_exp_f32_e32 v5, v5
	v_exp_f32_e32 v181, v181
	v_exp_f32_e32 v182, v182
	v_exp_f32_e32 v183, v183
	v_exp_f32_e32 v186, v186
	v_exp_f32_e32 v184, v184
	v_exp_f32_e32 v187, v187
	v_exp_f32_e32 v185, v185
	v_add_f32_e32 v5, 1.0, v5
	v_add_f32_e32 v181, 1.0, v181
	v_add_f32_e32 v188, 1.0, v182
	v_add_f32_e32 v189, 1.0, v183
	v_add_f32_e32 v186, 1.0, v186
	v_add_f32_e32 v190, 1.0, v184
	v_add_f32_e32 v191, 1.0, v187
	v_add_f32_e32 v192, 1.0, v185
	v_rcp_f32_e32 v182, v5
	v_rcp_f32_e32 v183, v181
	v_rcp_f32_e32 v184, v188
	v_rcp_f32_e32 v185, v189
	v_rcp_f32_e32 v186, v186
	v_rcp_f32_e32 v187, v190
	v_rcp_f32_e32 v188, v191
	v_rcp_f32_e32 v189, v192
	v_pk_mul_f32 v[160:161], v[160:161], v[182:183]
	v_pk_mul_f32 v[162:163], v[162:163], v[184:185]
	v_pk_mul_f32 v[156:157], v[156:157], v[186:187]
	v_pk_mul_f32 v[158:159], v[158:159], v[188:189]
	v_pk_mul_f32 v[56:57], v[56:57], v[162:163]
	v_pk_mul_f32 v[54:55], v[54:55], v[160:161]
	v_pk_mul_f32 v[52:53], v[52:53], v[158:159]
	v_pk_mul_f32 v[50:51], v[50:51], v[156:157]
.LBB0_613:
	global_load_dwordx4 v[156:159], v[8:9], off offset:64 nt
	s_and_b64 vcc, exec, s[4:5]
	s_mov_b64 s[58:59], -1
	s_waitcnt vmcnt(0)
	v_lshlrev_b32_e32 v5, 16, v156
	v_and_b32_e32 v8, 0xffff0000, v156
	v_lshlrev_b32_e32 v9, 16, v157
	v_and_b32_e32 v156, 0xffff0000, v157
	v_lshlrev_b32_e32 v157, 16, v158
	v_and_b32_e32 v158, 0xffff0000, v158
	v_lshlrev_b32_e32 v160, 16, v159
	v_and_b32_e32 v159, 0xffff0000, v159
	v_mul_f32_e32 v5, 0xbfb8aa3b, v5
	v_mul_f32_e32 v8, 0xbfb8aa3b, v8
	v_mul_f32_e32 v9, 0xbfb8aa3b, v9
	v_mul_f32_e32 v156, 0xbfb8aa3b, v156
	v_mul_f32_e32 v157, 0xbfb8aa3b, v157
	v_mul_f32_e32 v162, 0xbfb8aa3b, v158
	v_mul_f32_e32 v163, 0xbfb8aa3b, v160
	v_mul_f32_e32 v181, 0xbfb8aa3b, v159
	v_exp_f32_e32 v158, v5
	v_exp_f32_e32 v159, v8
	v_exp_f32_e32 v160, v9
	v_exp_f32_e32 v161, v156
	v_exp_f32_e32 v8, v157
	v_exp_f32_e32 v9, v162
	v_exp_f32_e32 v156, v163
	v_exp_f32_e32 v157, v181
	s_cbranch_vccnz .LBB0_636
	v_add_f32_e32 v162, 1.0, v159
	v_add_f32_e32 v163, 1.0, v160
	v_rcp_f32_e32 v162, v162
	v_rcp_f32_e32 v163, v163
	v_add_f32_e32 v182, 1.0, v8
	v_rcp_f32_e32 v182, v182
	v_mul_f32_e32 v162, v23, v162
	v_mul_f32_e32 v181, 0x3c000000, v162
	v_mul_f32_e32 v162, v24, v163
	v_add_f32_e32 v163, 1.0, v161
	v_rcp_f32_e32 v163, v163
	v_mul_f32_e32 v183, 0x3c000000, v162
	v_add_f32_e32 v5, 1.0, v158
	v_rcp_f32_e32 v5, v5
	v_mul_f32_e32 v162, v25, v163
	v_add_f32_e32 v163, 1.0, v9
	v_mul_f32_e32 v184, 0x3c000000, v162
	v_mul_f32_e32 v162, v18, v182
	v_rcp_f32_e32 v163, v163
	v_add_f32_e32 v182, 1.0, v156
	v_rcp_f32_e32 v182, v182
	v_mul_f32_e32 v185, 0x3c000000, v162
	v_mul_f32_e32 v162, v19, v163
	v_mul_f32_e32 v186, 0x3c000000, v162
	v_mul_f32_e32 v162, v20, v182
	v_mul_f32_e32 v182, 0x3c000000, v162
	v_add_f32_e32 v162, 1.0, v157
	v_mul_f32_e32 v5, v22, v5
	v_rcp_f32_e32 v187, v162
	v_mul_f32_e32 v5, 0x3c000000, v5
	v_mov_b32_e32 v162, 0
	v_mov_b32_e32 v163, 0
	v_cvt_pk_fp8_f32 v162, v5, v181
	v_cvt_pk_fp8_f32 v163, v185, v186
	v_mul_f32_e32 v5, v21, v187
	v_mul_f32_e32 v5, 0x3c000000, v5
	v_cvt_pk_fp8_f32 v162, v183, v184 op_sel:[0,0,1]
	v_cvt_pk_fp8_f32 v163, v182, v5 op_sel:[0,0,1]
	ds_write_b64 v180, v[162:163] offset:32
	s_cbranch_execz .LBB0_637

; #define LAS __attribute__((address_space(3)))
; __device__ __forceinline__ unsigned pk4_fp8(float a, float b, float c, float d) { int w = 0; w = __builtin_amdgcn_cvt_pk_fp8_f32(a, b, w, false); w = __builtin_amdgcn_cvt_pk_fp8_f32(c, d, w, true); return (unsigned)w; }
; __device__ __forceinline__ float bf_lo(unsigned w) { return __uint_as_float(w << 16); }
; __device__ __forceinline__ float bf_hi(unsigned w) { return __uint_as_float(w & 0xffff0000u); }
; __device__ __forceinline__ float sigmoidf_fast(float x) { return __builtin_amdgcn_rcpf(1.0f + __builtin_amdgcn_exp2f(-1.4426950408889634f * x)); }
;     __device__ __forceinline__ void operator()(f32x4 (&acc)[2][2][4][2], const Unit& u, int wr, int wc, int fr, int fq) const {
;     ...
;                 const size_t ro = (size_t)(u.row0 + ai * 128 + wr * 64 + m * 16 + fr) * DM + col0;
; #pragma unroll
;                 for (int bj = 0; bj < 2; ++bj) {
;                     const u32x4 gd = *(const u32x4*)(GDF + ro + bj * 32);
;                     const float ed[8] = {bf_lo(gd.x), bf_hi(gd.x), bf_lo(gd.y), bf_hi(gd.y), bf_lo(gd.z), bf_hi(gd.z), bf_lo(gd.w), bf_hi(gd.w)};
;                     if (u.tag == 0) {
;                         const u32x4 gn = *(const u32x4*)(GNA + ro + bj * 32);
;                         const float en[8] = {bf_lo(gn.x), bf_hi(gn.x), bf_lo(gn.y), bf_hi(gn.y), bf_lo(gn.z), bf_hi(gn.z), bf_lo(gn.w), bf_hi(gn.w)};
; #pragma unroll
;                         for (int e = 0; e < 8; ++e) {
;                             const float r = (1.0f + __builtin_amdgcn_exp2f(-1.4426950408889634f * ed[e])) * __builtin_amdgcn_rcpf(1.0f + __builtin_amdgcn_exp2f(-1.4426950408889634f * en[e]));
;                             acc[ai][bj][m][e >> 2][e & 3] *= r; }
;                     } else {
;                         float y[8];
; #pragma unroll
;                         for (int e = 0; e < 8; ++e) y[e] = acc[ai][bj][m][e >> 2][e & 3] * sigmoidf_fast(ed[e]) * (PSCALE * WSCALE_INV * OSCALE_INV);
;                         u32x2 w; w.x = pk4_fp8(y[0], y[1], y[2], y[3]); w.y = pk4_fp8(y[4], y[5], y[6], y[7]);
;                         *(LAS u32x2*)(my + fr * 80 + bj * 32 + fq * 8) = w;
;                     }
.LBB0_617:
	v_add_u32_e32 v4, 0xb0, v4
	v_ashrrev_i32_e32 v5, 31, v4
	v_lshlrev_b64 v[4:5], 11, v[4:5]
	v_lshl_add_u64 v[2:3], v[4:5], 0, v[2:3]
	v_lshl_add_u64 v[4:5], v[2:3], 1, s[40:41]
	global_load_dwordx4 v[6:9], v[4:5], off nt
	s_and_b64 vcc, exec, s[4:5]
	s_mov_b64 s[58:59], -1
	s_waitcnt vmcnt(0)
	v_lshlrev_b32_e32 v156, 16, v6
	v_and_b32_e32 v6, 0xffff0000, v6
	v_lshlrev_b32_e32 v157, 16, v7
	v_and_b32_e32 v7, 0xffff0000, v7
	v_lshlrev_b32_e32 v158, 16, v8
	v_and_b32_e32 v8, 0xffff0000, v8
	v_lshlrev_b32_e32 v159, 16, v9
	v_and_b32_e32 v9, 0xffff0000, v9
	v_mul_f32_e32 v156, 0xbfb8aa3b, v156
	v_mul_f32_e32 v6, 0xbfb8aa3b, v6
	v_mul_f32_e32 v160, 0xbfb8aa3b, v157
	v_mul_f32_e32 v7, 0xbfb8aa3b, v7
	v_mul_f32_e32 v161, 0xbfb8aa3b, v158
	v_mul_f32_e32 v8, 0xbfb8aa3b, v8
	v_mul_f32_e32 v162, 0xbfb8aa3b, v159
	v_mul_f32_e32 v9, 0xbfb8aa3b, v9
	v_exp_f32_e32 v156, v156
	v_exp_f32_e32 v157, v6
	v_exp_f32_e32 v158, v160
	v_exp_f32_e32 v159, v7
	v_exp_f32_e32 v6, v161
	v_exp_f32_e32 v7, v8
	v_exp_f32_e32 v8, v162
	v_exp_f32_e32 v9, v9
	s_cbranch_vccnz .LBB0_619
	v_add_f32_e32 v160, 1.0, v156
	v_rcp_f32_e32 v160, v160
	v_add_f32_e32 v161, 1.0, v157
	v_add_f32_e32 v162, 1.0, v158
	v_rcp_f32_e32 v161, v161
	v_rcp_f32_e32 v162, v162
	v_mul_f32_e32 v160, v46, v160
	v_mul_f32_e32 v163, 0x3c000000, v160
	v_mul_f32_e32 v160, v47, v161
	v_mul_f32_e32 v161, 0x3c000000, v160
	v_mul_f32_e32 v160, v48, v162
	v_add_f32_e32 v162, 1.0, v159
	v_rcp_f32_e32 v162, v162
	v_add_f32_e32 v181, 1.0, v6
	v_rcp_f32_e32 v181, v181
	v_mul_f32_e32 v182, 0x3c000000, v160
	v_mul_f32_e32 v160, v49, v162
	v_mul_f32_e32 v162, 0x3c000000, v160
	v_mul_f32_e32 v160, v42, v181
	v_add_f32_e32 v181, 1.0, v7
	v_rcp_f32_e32 v181, v181
	v_add_f32_e32 v183, 1.0, v8
	v_rcp_f32_e32 v183, v183
	v_mul_f32_e32 v184, 0x3c000000, v160
	v_mul_f32_e32 v160, v43, v181
	v_mul_f32_e32 v181, 0x3c000000, v160
	v_mul_f32_e32 v160, v44, v183
	v_mul_f32_e32 v183, 0x3c000000, v160
	v_add_f32_e32 v160, 1.0, v9
	v_rcp_f32_e32 v185, v160
	v_mov_b32_e32 v160, 0
	v_cvt_pk_fp8_f32 v160, v163, v161
	v_mov_b32_e32 v161, 0
	v_cvt_pk_fp8_f32 v161, v184, v181
	v_mul_f32_e32 v163, v45, v185
	v_mul_f32_e32 v163, 0x3c000000, v163
	v_cvt_pk_fp8_f32 v160, v182, v162 op_sel:[0,0,1]
	v_cvt_pk_fp8_f32 v161, v183, v163 op_sel:[0,0,1]
	s_mov_b64 s[58:59], 0
	ds_write_b64 v180, v[160:161]
.LBB0_619:
	s_andn2_b64 vcc, exec, s[58:59]
	v_lshl_add_u64 v[2:3], v[2:3], 1, s[38:39]
	s_cbranch_vccnz .LBB0_621
	global_load_dwordx4 v[160:163], v[2:3], off nt
	v_pk_add_f32 v[158:159], v[158:159], 1.0 op_sel_hi:[1,0]
	v_pk_add_f32 v[156:157], v[156:157], 1.0 op_sel_hi:[1,0]
	v_pk_add_f32 v[8:9], v[8:9], 1.0 op_sel_hi:[1,0]
	v_pk_add_f32 v[6:7], v[6:7], 1.0 op_sel_hi:[1,0]
	s_waitcnt vmcnt(0)
	v_lshlrev_b32_e32 v181, 16, v160
	v_and_b32_e32 v160, 0xffff0000, v160
	v_lshlrev_b32_e32 v182, 16, v161
	v_and_b32_e32 v161, 0xffff0000, v161
	v_lshlrev_b32_e32 v183, 16, v162
	v_and_b32_e32 v162, 0xffff0000, v162
	v_lshlrev_b32_e32 v184, 16, v163
	v_and_b32_e32 v163, 0xffff0000, v163
	v_mul_f32_e32 v181, 0xbfb8aa3b, v181
	v_mul_f32_e32 v160, 0xbfb8aa3b, v160
	v_mul_f32_e32 v182, 0xbfb8aa3b, v182
	v_mul_f32_e32 v161, 0xbfb8aa3b, v161
	v_mul_f32_e32 v183, 0xbfb8aa3b, v183
	v_mul_f32_e32 v162, 0xbfb8aa3b, v162
	v_mul_f32_e32 v184, 0xbfb8aa3b, v184
	v_mul_f32_e32 v163, 0xbfb8aa3b, v163
	v_exp_f32_e32 v181, v181
	v_exp_f32_e32 v160, v160
	v_exp_f32_e32 v182, v182
	v_exp_f32_e32 v161, v161
	v_exp_f32_e32 v183, v183
	v_exp_f32_e32 v162, v162
	v_exp_f32_e32 v184, v184
	v_exp_f32_e32 v163, v163
	v_add_f32_e32 v181, 1.0, v181
	v_add_f32_e32 v185, 1.0, v160
	v_add_f32_e32 v182, 1.0, v182
	v_add_f32_e32 v186, 1.0, v161
	v_add_f32_e32 v183, 1.0, v183
	v_add_f32_e32 v187, 1.0, v162
	v_add_f32_e32 v184, 1.0, v184
	v_add_f32_e32 v188, 1.0, v163
	v_rcp_f32_e32 v160, v181
	v_rcp_f32_e32 v161, v185
	v_rcp_f32_e32 v162, v182
	v_rcp_f32_e32 v163, v186
	v_rcp_f32_e32 v182, v183
	v_rcp_f32_e32 v183, v187
	v_rcp_f32_e32 v184, v184
	v_rcp_f32_e32 v185, v188
	v_pk_mul_f32 v[156:157], v[156:157], v[160:161]
	v_pk_mul_f32 v[158:159], v[158:159], v[162:163]
	v_pk_mul_f32 v[6:7], v[6:7], v[182:183]
	v_pk_mul_f32 v[8:9], v[8:9], v[184:185]
	v_pk_mul_f32 v[48:49], v[48:49], v[158:159]
	v_pk_mul_f32 v[46:47], v[46:47], v[156:157]
	v_pk_mul_f32 v[44:45], v[44:45], v[8:9]
	v_pk_mul_f32 v[42:43], v[42:43], v[6:7]
.LBB0_621:
	global_load_dwordx4 v[4:7], v[4:5], off offset:64 nt
	s_and_b64 vcc, exec, s[4:5]
	s_mov_b64 s[4:5], -1
	s_waitcnt vmcnt(0)
	v_lshlrev_b32_e32 v8, 16, v4
	v_and_b32_e32 v4, 0xffff0000, v4
	v_lshlrev_b32_e32 v9, 16, v5
	v_and_b32_e32 v5, 0xffff0000, v5
	v_lshlrev_b32_e32 v156, 16, v6
	v_and_b32_e32 v6, 0xffff0000, v6
	v_lshlrev_b32_e32 v157, 16, v7
	v_and_b32_e32 v7, 0xffff0000, v7
	v_mul_f32_e32 v8, 0xbfb8aa3b, v8
	v_mul_f32_e32 v4, 0xbfb8aa3b, v4
	v_mul_f32_e32 v158, 0xbfb8aa3b, v9
	v_mul_f32_e32 v5, 0xbfb8aa3b, v5
	v_mul_f32_e32 v159, 0xbfb8aa3b, v156
	v_mul_f32_e32 v6, 0xbfb8aa3b, v6
	v_mul_f32_e32 v160, 0xbfb8aa3b, v157
	v_mul_f32_e32 v7, 0xbfb8aa3b, v7
	v_exp_f32_e32 v8, v8
	v_exp_f32_e32 v9, v4
	v_exp_f32_e32 v156, v158
	v_exp_f32_e32 v157, v5
	v_exp_f32_e32 v4, v159
	v_exp_f32_e32 v5, v6
	v_exp_f32_e32 v6, v160
	v_exp_f32_e32 v7, v7
	s_cbranch_vccnz .LBB0_638
	v_add_f32_e32 v158, 1.0, v8
	v_rcp_f32_e32 v158, v158
	v_add_f32_e32 v159, 1.0, v9
	v_add_f32_e32 v160, 1.0, v156
	v_rcp_f32_e32 v159, v159
	v_rcp_f32_e32 v160, v160
	v_mul_f32_e32 v158, v14, v158
	v_mul_f32_e32 v161, 0x3c000000, v158
	v_mul_f32_e32 v158, v15, v159
	v_mul_f32_e32 v159, 0x3c000000, v158
	v_mul_f32_e32 v158, v16, v160
	v_add_f32_e32 v160, 1.0, v157
	v_rcp_f32_e32 v160, v160
	v_add_f32_e32 v162, 1.0, v4
	v_rcp_f32_e32 v162, v162
	v_mul_f32_e32 v163, 0x3c000000, v158
	v_mul_f32_e32 v158, v17, v160
	v_mul_f32_e32 v160, 0x3c000000, v158
	v_mul_f32_e32 v158, v10, v162
	v_add_f32_e32 v162, 1.0, v5
	v_rcp_f32_e32 v162, v162
	v_add_f32_e32 v181, 1.0, v6
	v_rcp_f32_e32 v181, v181
	v_mul_f32_e32 v182, 0x3c000000, v158
	v_mul_f32_e32 v158, v11, v162
	v_mul_f32_e32 v162, 0x3c000000, v158
	v_mul_f32_e32 v158, v12, v181
	v_mul_f32_e32 v181, 0x3c000000, v158
	v_add_f32_e32 v158, 1.0, v7
	v_rcp_f32_e32 v183, v158
	v_mov_b32_e32 v158, 0
	v_cvt_pk_fp8_f32 v158, v161, v159
	v_mov_b32_e32 v159, 0
	v_cvt_pk_fp8_f32 v159, v182, v162
	v_mul_f32_e32 v161, v13, v183
	v_mul_f32_e32 v161, 0x3c000000, v161
	v_cvt_pk_fp8_f32 v158, v163, v160 op_sel:[0,0,1]
	v_cvt_pk_fp8_f32 v159, v181, v161 op_sel:[0,0,1]
	ds_write_b64 v180, v[158:159] offset:32
	s_cbranch_execz .LBB0_639

; __device__ __forceinline__ float bf_lo(unsigned w) { return __uint_as_float(w << 16); }
; __device__ __forceinline__ float bf_hi(unsigned w) { return __uint_as_float(w & 0xffff0000u); }
;     __device__ __forceinline__ void operator()(f32x4 (&acc)[2][2][4][2], const Unit& u, int wr, int wc, int fr, int fq) const {
;     ...
;                     if (u.tag == 0) {
;                         const u32x4 gn = *(const u32x4*)(GNA + ro + bj * 32);
;                         const float en[8] = {bf_lo(gn.x), bf_hi(gn.x), bf_lo(gn.y), bf_hi(gn.y), bf_lo(gn.z), bf_hi(gn.z), bf_lo(gn.w), bf_hi(gn.w)};
; #pragma unroll
;                         for (int e = 0; e < 8; ++e) {
;                             const float r = (1.0f + __builtin_amdgcn_exp2f(-1.4426950408889634f * ed[e])) * __builtin_amdgcn_rcpf(1.0f + __builtin_amdgcn_exp2f(-1.4426950408889634f * en[e]));
;                             acc[ai][bj][m][e >> 2][e & 3] *= r; }
.LBB0_625:
	global_load_dwordx4 v[182:185], v[8:9], off offset:64 nt
	v_pk_add_f32 v[8:9], v[160:161], 1.0 op_sel_hi:[1,0]
	v_pk_add_f32 v[158:159], v[158:159], 1.0 op_sel_hi:[1,0]
	v_pk_add_f32 v[156:157], v[156:157], 1.0 op_sel_hi:[1,0]
	v_pk_add_f32 v[6:7], v[6:7], 1.0 op_sel_hi:[1,0]
	s_waitcnt vmcnt(0)
	v_lshlrev_b32_e32 v5, 16, v182
	v_and_b32_e32 v160, 0xffff0000, v182
	v_lshlrev_b32_e32 v161, 16, v183
	v_and_b32_e32 v162, 0xffff0000, v183
	v_lshlrev_b32_e32 v163, 16, v184
	v_and_b32_e32 v181, 0xffff0000, v184
	v_lshlrev_b32_e32 v182, 16, v185
	v_and_b32_e32 v183, 0xffff0000, v185
	v_mul_f32_e32 v5, 0xbfb8aa3b, v5
	v_mul_f32_e32 v160, 0xbfb8aa3b, v160
	v_mul_f32_e32 v161, 0xbfb8aa3b, v161
	v_mul_f32_e32 v162, 0xbfb8aa3b, v162
	v_mul_f32_e32 v163, 0xbfb8aa3b, v163
	v_mul_f32_e32 v181, 0xbfb8aa3b, v181
	v_mul_f32_e32 v182, 0xbfb8aa3b, v182
	v_mul_f32_e32 v183, 0xbfb8aa3b, v183
	v_exp_f32_e32 v5, v5
	v_exp_f32_e32 v160, v160
	v_exp_f32_e32 v161, v161
	v_exp_f32_e32 v162, v162
	v_exp_f32_e32 v163, v163
	v_exp_f32_e32 v181, v181
	v_exp_f32_e32 v182, v182
	v_exp_f32_e32 v183, v183
	v_add_f32_e32 v5, 1.0, v5
	v_add_f32_e32 v184, 1.0, v160
	v_add_f32_e32 v185, 1.0, v161
	v_add_f32_e32 v186, 1.0, v162
	v_add_f32_e32 v187, 1.0, v163
	v_add_f32_e32 v181, 1.0, v181
	v_add_f32_e32 v188, 1.0, v182
	v_add_f32_e32 v189, 1.0, v183
	v_rcp_f32_e32 v160, v5
	v_rcp_f32_e32 v161, v184
	v_rcp_f32_e32 v162, v185
	v_rcp_f32_e32 v163, v186
	v_rcp_f32_e32 v182, v187
	v_rcp_f32_e32 v183, v181
	v_rcp_f32_e32 v184, v188
	v_rcp_f32_e32 v185, v189
	v_pk_mul_f32 v[158:159], v[158:159], v[160:161]
	v_pk_mul_f32 v[8:9], v[8:9], v[162:163]
	v_pk_mul_f32 v[6:7], v[6:7], v[182:183]
	v_pk_mul_f32 v[156:157], v[156:157], v[184:185]
	v_pk_mul_f32 v[104:105], v[104:105], v[8:9]
	v_pk_mul_f32 v[102:103], v[102:103], v[158:159]
	v_pk_mul_f32 v[100:101], v[100:101], v[156:157]
	v_pk_mul_f32 v[98:99], v[98:99], v[6:7]
	s_and_b64 vcc, exec, s[4:5]
	s_cbranch_vccz .LBB0_568
	s_branch .LBB0_569

; __device__ __forceinline__ float bf_lo(unsigned w) { return __uint_as_float(w << 16); }
; __device__ __forceinline__ float bf_hi(unsigned w) { return __uint_as_float(w & 0xffff0000u); }
;     __device__ __forceinline__ void operator()(f32x4 (&acc)[2][2][4][2], const Unit& u, int wr, int wc, int fr, int fq) const {
;     ...
;                     if (u.tag == 0) {
;                         const u32x4 gn = *(const u32x4*)(GNA + ro + bj * 32);
;                         const float en[8] = {bf_lo(gn.x), bf_hi(gn.x), bf_lo(gn.y), bf_hi(gn.y), bf_lo(gn.z), bf_hi(gn.z), bf_lo(gn.w), bf_hi(gn.w)};
; #pragma unroll
;                         for (int e = 0; e < 8; ++e) {
;                             const float r = (1.0f + __builtin_amdgcn_exp2f(-1.4426950408889634f * ed[e])) * __builtin_amdgcn_rcpf(1.0f + __builtin_amdgcn_exp2f(-1.4426950408889634f * en[e]));
;                             acc[ai][bj][m][e >> 2][e & 3] *= r; }
.LBB0_627:
	global_load_dwordx4 v[182:185], v[6:7], off offset:64 nt
	v_pk_add_f32 v[6:7], v[160:161], 1.0 op_sel_hi:[1,0]
	v_pk_add_f32 v[158:159], v[158:159], 1.0 op_sel_hi:[1,0]
	v_pk_add_f32 v[156:157], v[156:157], 1.0 op_sel_hi:[1,0]
	v_pk_add_f32 v[8:9], v[8:9], 1.0 op_sel_hi:[1,0]
	s_waitcnt vmcnt(0)
	v_lshlrev_b32_e32 v5, 16, v182
	v_and_b32_e32 v160, 0xffff0000, v182
	v_lshlrev_b32_e32 v161, 16, v183
	v_and_b32_e32 v162, 0xffff0000, v183
	v_lshlrev_b32_e32 v163, 16, v184
	v_and_b32_e32 v181, 0xffff0000, v184
	v_lshlrev_b32_e32 v182, 16, v185
	v_and_b32_e32 v183, 0xffff0000, v185
	v_mul_f32_e32 v5, 0xbfb8aa3b, v5
	v_mul_f32_e32 v160, 0xbfb8aa3b, v160
	v_mul_f32_e32 v161, 0xbfb8aa3b, v161
	v_mul_f32_e32 v162, 0xbfb8aa3b, v162
	v_mul_f32_e32 v163, 0xbfb8aa3b, v163
	v_mul_f32_e32 v181, 0xbfb8aa3b, v181
	v_mul_f32_e32 v182, 0xbfb8aa3b, v182
	v_mul_f32_e32 v183, 0xbfb8aa3b, v183
	v_exp_f32_e32 v5, v5
	v_exp_f32_e32 v160, v160
	v_exp_f32_e32 v161, v161
	v_exp_f32_e32 v162, v162
	v_exp_f32_e32 v163, v163
	v_exp_f32_e32 v181, v181
	v_exp_f32_e32 v182, v182
	v_exp_f32_e32 v183, v183
	v_add_f32_e32 v5, 1.0, v5
	v_add_f32_e32 v184, 1.0, v160
	v_add_f32_e32 v185, 1.0, v161
	v_add_f32_e32 v186, 1.0, v162
	v_add_f32_e32 v187, 1.0, v163
	v_add_f32_e32 v181, 1.0, v181
	v_add_f32_e32 v188, 1.0, v182
	v_add_f32_e32 v189, 1.0, v183
	v_rcp_f32_e32 v160, v5
	v_rcp_f32_e32 v161, v184
	v_rcp_f32_e32 v162, v185
	v_rcp_f32_e32 v163, v186
	v_rcp_f32_e32 v182, v187
	v_rcp_f32_e32 v183, v181
	v_rcp_f32_e32 v184, v188
	v_rcp_f32_e32 v185, v189
	v_pk_mul_f32 v[158:159], v[158:159], v[160:161]
	v_pk_mul_f32 v[6:7], v[6:7], v[162:163]
	v_pk_mul_f32 v[8:9], v[8:9], v[182:183]
	v_pk_mul_f32 v[156:157], v[156:157], v[184:185]
	v_pk_mul_f32 v[96:97], v[96:97], v[6:7]
	v_pk_mul_f32 v[94:95], v[94:95], v[158:159]
	v_pk_mul_f32 v[92:93], v[92:93], v[156:157]
	v_pk_mul_f32 v[90:91], v[90:91], v[8:9]
	s_and_b64 vcc, exec, s[4:5]
	s_cbranch_vccz .LBB0_576
	s_branch .LBB0_577

; __device__ __forceinline__ float bf_lo(unsigned w) { return __uint_as_float(w << 16); }
; __device__ __forceinline__ float bf_hi(unsigned w) { return __uint_as_float(w & 0xffff0000u); }
;     __device__ __forceinline__ void operator()(f32x4 (&acc)[2][2][4][2], const Unit& u, int wr, int wc, int fr, int fq) const {
;     ...
;                     if (u.tag == 0) {
;                         const u32x4 gn = *(const u32x4*)(GNA + ro + bj * 32);
;                         const float en[8] = {bf_lo(gn.x), bf_hi(gn.x), bf_lo(gn.y), bf_hi(gn.y), bf_lo(gn.z), bf_hi(gn.z), bf_lo(gn.w), bf_hi(gn.w)};
; #pragma unroll
;                         for (int e = 0; e < 8; ++e) {
;                             const float r = (1.0f + __builtin_amdgcn_exp2f(-1.4426950408889634f * ed[e])) * __builtin_amdgcn_rcpf(1.0f + __builtin_amdgcn_exp2f(-1.4426950408889634f * en[e]));
;                             acc[ai][bj][m][e >> 2][e & 3] *= r; }
.LBB0_629:
	global_load_dwordx4 v[182:185], v[6:7], off offset:64 nt
	v_pk_add_f32 v[6:7], v[160:161], 1.0 op_sel_hi:[1,0]
	v_pk_add_f32 v[158:159], v[158:159], 1.0 op_sel_hi:[1,0]
	v_pk_add_f32 v[156:157], v[156:157], 1.0 op_sel_hi:[1,0]
	v_pk_add_f32 v[8:9], v[8:9], 1.0 op_sel_hi:[1,0]
	s_waitcnt vmcnt(0)
	v_lshlrev_b32_e32 v5, 16, v182
	v_and_b32_e32 v160, 0xffff0000, v182
	v_lshlrev_b32_e32 v161, 16, v183
	v_and_b32_e32 v162, 0xffff0000, v183
	v_lshlrev_b32_e32 v163, 16, v184
	v_and_b32_e32 v181, 0xffff0000, v184
	v_lshlrev_b32_e32 v182, 16, v185
	v_and_b32_e32 v183, 0xffff0000, v185
	v_mul_f32_e32 v5, 0xbfb8aa3b, v5
	v_mul_f32_e32 v160, 0xbfb8aa3b, v160
	v_mul_f32_e32 v161, 0xbfb8aa3b, v161
	v_mul_f32_e32 v162, 0xbfb8aa3b, v162
	v_mul_f32_e32 v163, 0xbfb8aa3b, v163
	v_mul_f32_e32 v181, 0xbfb8aa3b, v181
	v_mul_f32_e32 v182, 0xbfb8aa3b, v182
	v_mul_f32_e32 v183, 0xbfb8aa3b, v183
	v_exp_f32_e32 v5, v5
	v_exp_f32_e32 v160, v160
	v_exp_f32_e32 v161, v161
	v_exp_f32_e32 v162, v162
	v_exp_f32_e32 v163, v163
	v_exp_f32_e32 v181, v181
	v_exp_f32_e32 v182, v182
	v_exp_f32_e32 v183, v183
	v_add_f32_e32 v5, 1.0, v5
	v_add_f32_e32 v184, 1.0, v160
	v_add_f32_e32 v185, 1.0, v161
	v_add_f32_e32 v186, 1.0, v162
	v_add_f32_e32 v187, 1.0, v163
	v_add_f32_e32 v181, 1.0, v181
	v_add_f32_e32 v188, 1.0, v182
	v_add_f32_e32 v189, 1.0, v183
	v_rcp_f32_e32 v160, v5
	v_rcp_f32_e32 v161, v184
	v_rcp_f32_e32 v162, v185
	v_rcp_f32_e32 v163, v186
	v_rcp_f32_e32 v182, v187
	v_rcp_f32_e32 v183, v181
	v_rcp_f32_e32 v184, v188
	v_rcp_f32_e32 v185, v189
	v_pk_mul_f32 v[158:159], v[158:159], v[160:161]
	v_pk_mul_f32 v[6:7], v[6:7], v[162:163]
	v_pk_mul_f32 v[8:9], v[8:9], v[182:183]
	v_pk_mul_f32 v[156:157], v[156:157], v[184:185]
	v_pk_mul_f32 v[88:89], v[88:89], v[6:7]
	v_pk_mul_f32 v[86:87], v[86:87], v[158:159]
	v_pk_mul_f32 v[84:85], v[84:85], v[156:157]
	v_pk_mul_f32 v[82:83], v[82:83], v[8:9]
	s_and_b64 vcc, exec, s[4:5]
	s_cbranch_vccz .LBB0_584
	s_branch .LBB0_585

; __device__ __forceinline__ float bf_lo(unsigned w) { return __uint_as_float(w << 16); }
; __device__ __forceinline__ float bf_hi(unsigned w) { return __uint_as_float(w & 0xffff0000u); }
;     __device__ __forceinline__ void operator()(f32x4 (&acc)[2][2][4][2], const Unit& u, int wr, int wc, int fr, int fq) const {
;     ...
;                     if (u.tag == 0) {
;                         const u32x4 gn = *(const u32x4*)(GNA + ro + bj * 32);
;                         const float en[8] = {bf_lo(gn.x), bf_hi(gn.x), bf_lo(gn.y), bf_hi(gn.y), bf_lo(gn.z), bf_hi(gn.z), bf_lo(gn.w), bf_hi(gn.w)};
; #pragma unroll
;                         for (int e = 0; e < 8; ++e) {
;                             const float r = (1.0f + __builtin_amdgcn_exp2f(-1.4426950408889634f * ed[e])) * __builtin_amdgcn_rcpf(1.0f + __builtin_amdgcn_exp2f(-1.4426950408889634f * en[e]));
;                             acc[ai][bj][m][e >> 2][e & 3] *= r; }
.LBB0_631:
	global_load_dwordx4 v[182:185], v[6:7], off offset:64 nt
	v_pk_add_f32 v[6:7], v[160:161], 1.0 op_sel_hi:[1,0]
	v_pk_add_f32 v[158:159], v[158:159], 1.0 op_sel_hi:[1,0]
	v_pk_add_f32 v[156:157], v[156:157], 1.0 op_sel_hi:[1,0]
	v_pk_add_f32 v[8:9], v[8:9], 1.0 op_sel_hi:[1,0]
	s_waitcnt vmcnt(0)
	v_lshlrev_b32_e32 v5, 16, v182
	v_and_b32_e32 v160, 0xffff0000, v182
	v_lshlrev_b32_e32 v161, 16, v183
	v_and_b32_e32 v162, 0xffff0000, v183
	v_lshlrev_b32_e32 v163, 16, v184
	v_and_b32_e32 v181, 0xffff0000, v184
	v_lshlrev_b32_e32 v182, 16, v185
	v_and_b32_e32 v183, 0xffff0000, v185
	v_mul_f32_e32 v5, 0xbfb8aa3b, v5
	v_mul_f32_e32 v160, 0xbfb8aa3b, v160
	v_mul_f32_e32 v161, 0xbfb8aa3b, v161
	v_mul_f32_e32 v162, 0xbfb8aa3b, v162
	v_mul_f32_e32 v163, 0xbfb8aa3b, v163
	v_mul_f32_e32 v181, 0xbfb8aa3b, v181
	v_mul_f32_e32 v182, 0xbfb8aa3b, v182
	v_mul_f32_e32 v183, 0xbfb8aa3b, v183
	v_exp_f32_e32 v5, v5
	v_exp_f32_e32 v160, v160
	v_exp_f32_e32 v161, v161
	v_exp_f32_e32 v162, v162
	v_exp_f32_e32 v163, v163
	v_exp_f32_e32 v181, v181
	v_exp_f32_e32 v182, v182
	v_exp_f32_e32 v183, v183
	v_add_f32_e32 v5, 1.0, v5
	v_add_f32_e32 v184, 1.0, v160
	v_add_f32_e32 v185, 1.0, v161
	v_add_f32_e32 v186, 1.0, v162
	v_add_f32_e32 v187, 1.0, v163
	v_add_f32_e32 v181, 1.0, v181
	v_add_f32_e32 v188, 1.0, v182
	v_add_f32_e32 v189, 1.0, v183
	v_rcp_f32_e32 v160, v5
	v_rcp_f32_e32 v161, v184
	v_rcp_f32_e32 v162, v185
	v_rcp_f32_e32 v163, v186
	v_rcp_f32_e32 v182, v187
	v_rcp_f32_e32 v183, v181
	v_rcp_f32_e32 v184, v188
	v_rcp_f32_e32 v185, v189
	v_pk_mul_f32 v[158:159], v[158:159], v[160:161]
	v_pk_mul_f32 v[6:7], v[6:7], v[162:163]
	v_pk_mul_f32 v[8:9], v[8:9], v[182:183]
	v_pk_mul_f32 v[156:157], v[156:157], v[184:185]
	v_pk_mul_f32 v[80:81], v[80:81], v[6:7]
	v_pk_mul_f32 v[78:79], v[78:79], v[158:159]
	v_pk_mul_f32 v[76:77], v[76:77], v[156:157]
	v_pk_mul_f32 v[74:75], v[74:75], v[8:9]
	s_and_b64 vcc, exec, s[4:5]
	s_cbranch_vccz .LBB0_592
	s_branch .LBB0_593

; __device__ __forceinline__ float bf_lo(unsigned w) { return __uint_as_float(w << 16); }
; __device__ __forceinline__ float bf_hi(unsigned w) { return __uint_as_float(w & 0xffff0000u); }
;     __device__ __forceinline__ void operator()(f32x4 (&acc)[2][2][4][2], const Unit& u, int wr, int wc, int fr, int fq) const {
;     ...
;                     if (u.tag == 0) {
;                         const u32x4 gn = *(const u32x4*)(GNA + ro + bj * 32);
;                         const float en[8] = {bf_lo(gn.x), bf_hi(gn.x), bf_lo(gn.y), bf_hi(gn.y), bf_lo(gn.z), bf_hi(gn.z), bf_lo(gn.w), bf_hi(gn.w)};
; #pragma unroll
;                         for (int e = 0; e < 8; ++e) {
;                             const float r = (1.0f + __builtin_amdgcn_exp2f(-1.4426950408889634f * ed[e])) * __builtin_amdgcn_rcpf(1.0f + __builtin_amdgcn_exp2f(-1.4426950408889634f * en[e]));
;                             acc[ai][bj][m][e >> 2][e & 3] *= r; }
.LBB0_633:
	global_load_dwordx4 v[182:185], v[6:7], off offset:64 nt
	v_pk_add_f32 v[6:7], v[160:161], 1.0 op_sel_hi:[1,0]
	v_pk_add_f32 v[158:159], v[158:159], 1.0 op_sel_hi:[1,0]
	v_pk_add_f32 v[156:157], v[156:157], 1.0 op_sel_hi:[1,0]
	v_pk_add_f32 v[8:9], v[8:9], 1.0 op_sel_hi:[1,0]
	s_waitcnt vmcnt(0)
	v_lshlrev_b32_e32 v5, 16, v182
	v_and_b32_e32 v160, 0xffff0000, v182
	v_lshlrev_b32_e32 v161, 16, v183
	v_and_b32_e32 v162, 0xffff0000, v183
	v_lshlrev_b32_e32 v163, 16, v184
	v_and_b32_e32 v181, 0xffff0000, v184
	v_lshlrev_b32_e32 v182, 16, v185
	v_and_b32_e32 v183, 0xffff0000, v185
	v_mul_f32_e32 v5, 0xbfb8aa3b, v5
	v_mul_f32_e32 v160, 0xbfb8aa3b, v160
	v_mul_f32_e32 v161, 0xbfb8aa3b, v161
	v_mul_f32_e32 v162, 0xbfb8aa3b, v162
	v_mul_f32_e32 v163, 0xbfb8aa3b, v163
	v_mul_f32_e32 v181, 0xbfb8aa3b, v181
	v_mul_f32_e32 v182, 0xbfb8aa3b, v182
	v_mul_f32_e32 v183, 0xbfb8aa3b, v183
	v_exp_f32_e32 v5, v5
	v_exp_f32_e32 v160, v160
	v_exp_f32_e32 v161, v161
	v_exp_f32_e32 v162, v162
	v_exp_f32_e32 v163, v163
	v_exp_f32_e32 v181, v181
	v_exp_f32_e32 v182, v182
	v_exp_f32_e32 v183, v183
	v_add_f32_e32 v5, 1.0, v5
	v_add_f32_e32 v184, 1.0, v160
	v_add_f32_e32 v185, 1.0, v161
	v_add_f32_e32 v186, 1.0, v162
	v_add_f32_e32 v187, 1.0, v163
	v_add_f32_e32 v181, 1.0, v181
	v_add_f32_e32 v188, 1.0, v182
	v_add_f32_e32 v189, 1.0, v183
	v_rcp_f32_e32 v160, v5
	v_rcp_f32_e32 v161, v184
	v_rcp_f32_e32 v162, v185
	v_rcp_f32_e32 v163, v186
	v_rcp_f32_e32 v182, v187
	v_rcp_f32_e32 v183, v181
	v_rcp_f32_e32 v184, v188
	v_rcp_f32_e32 v185, v189
	v_pk_mul_f32 v[158:159], v[158:159], v[160:161]
	v_pk_mul_f32 v[6:7], v[6:7], v[162:163]
	v_pk_mul_f32 v[8:9], v[8:9], v[182:183]
	v_pk_mul_f32 v[156:157], v[156:157], v[184:185]
	v_pk_mul_f32 v[40:41], v[40:41], v[6:7]
	v_pk_mul_f32 v[38:39], v[38:39], v[158:159]
	v_pk_mul_f32 v[36:37], v[36:37], v[156:157]
	v_pk_mul_f32 v[34:35], v[34:35], v[8:9]
	s_and_b64 vcc, exec, s[4:5]
	s_cbranch_vccz .LBB0_600
	s_branch .LBB0_601

; __device__ __forceinline__ float bf_lo(unsigned w) { return __uint_as_float(w << 16); }
; __device__ __forceinline__ float bf_hi(unsigned w) { return __uint_as_float(w & 0xffff0000u); }
;     __device__ __forceinline__ void operator()(f32x4 (&acc)[2][2][4][2], const Unit& u, int wr, int wc, int fr, int fq) const {
;     ...
;                     if (u.tag == 0) {
;                         const u32x4 gn = *(const u32x4*)(GNA + ro + bj * 32);
;                         const float en[8] = {bf_lo(gn.x), bf_hi(gn.x), bf_lo(gn.y), bf_hi(gn.y), bf_lo(gn.z), bf_hi(gn.z), bf_lo(gn.w), bf_hi(gn.w)};
; #pragma unroll
;                         for (int e = 0; e < 8; ++e) {
;                             const float r = (1.0f + __builtin_amdgcn_exp2f(-1.4426950408889634f * ed[e])) * __builtin_amdgcn_rcpf(1.0f + __builtin_amdgcn_exp2f(-1.4426950408889634f * en[e]));
;                             acc[ai][bj][m][e >> 2][e & 3] *= r; }
.LBB0_635:
	global_load_dwordx4 v[182:185], v[6:7], off offset:64 nt
	v_pk_add_f32 v[6:7], v[160:161], 1.0 op_sel_hi:[1,0]
	v_pk_add_f32 v[158:159], v[158:159], 1.0 op_sel_hi:[1,0]
	v_pk_add_f32 v[156:157], v[156:157], 1.0 op_sel_hi:[1,0]
	v_pk_add_f32 v[8:9], v[8:9], 1.0 op_sel_hi:[1,0]
	s_waitcnt vmcnt(0)
	v_lshlrev_b32_e32 v5, 16, v182
	v_and_b32_e32 v160, 0xffff0000, v182
	v_lshlrev_b32_e32 v161, 16, v183
	v_and_b32_e32 v162, 0xffff0000, v183
	v_lshlrev_b32_e32 v163, 16, v184
	v_and_b32_e32 v181, 0xffff0000, v184
	v_lshlrev_b32_e32 v182, 16, v185
	v_and_b32_e32 v183, 0xffff0000, v185
	v_mul_f32_e32 v5, 0xbfb8aa3b, v5
	v_mul_f32_e32 v160, 0xbfb8aa3b, v160
	v_mul_f32_e32 v161, 0xbfb8aa3b, v161
	v_mul_f32_e32 v162, 0xbfb8aa3b, v162
	v_mul_f32_e32 v163, 0xbfb8aa3b, v163
	v_mul_f32_e32 v181, 0xbfb8aa3b, v181
	v_mul_f32_e32 v182, 0xbfb8aa3b, v182
	v_mul_f32_e32 v183, 0xbfb8aa3b, v183
	v_exp_f32_e32 v5, v5
	v_exp_f32_e32 v160, v160
	v_exp_f32_e32 v161, v161
	v_exp_f32_e32 v162, v162
	v_exp_f32_e32 v163, v163
	v_exp_f32_e32 v181, v181
	v_exp_f32_e32 v182, v182
	v_exp_f32_e32 v183, v183
	v_add_f32_e32 v5, 1.0, v5
	v_add_f32_e32 v184, 1.0, v160
	v_add_f32_e32 v185, 1.0, v161
	v_add_f32_e32 v186, 1.0, v162
	v_add_f32_e32 v187, 1.0, v163
	v_add_f32_e32 v181, 1.0, v181
	v_add_f32_e32 v188, 1.0, v182
	v_add_f32_e32 v189, 1.0, v183
	v_rcp_f32_e32 v160, v5
	v_rcp_f32_e32 v161, v184
	v_rcp_f32_e32 v162, v185
	v_rcp_f32_e32 v163, v186
	v_rcp_f32_e32 v182, v187
	v_rcp_f32_e32 v183, v181
	v_rcp_f32_e32 v184, v188
	v_rcp_f32_e32 v185, v189
	v_pk_mul_f32 v[158:159], v[158:159], v[160:161]
	v_pk_mul_f32 v[6:7], v[6:7], v[162:163]
	v_pk_mul_f32 v[8:9], v[8:9], v[182:183]
	v_pk_mul_f32 v[156:157], v[156:157], v[184:185]
	v_pk_mul_f32 v[32:33], v[32:33], v[6:7]
	v_pk_mul_f32 v[30:31], v[30:31], v[158:159]
	v_pk_mul_f32 v[28:29], v[28:29], v[156:157]
	v_pk_mul_f32 v[26:27], v[26:27], v[8:9]
	s_and_b64 vcc, exec, s[4:5]
	s_cbranch_vccz .LBB0_608
	s_branch .LBB0_609

; __device__ __forceinline__ float bf_lo(unsigned w) { return __uint_as_float(w << 16); }
; __device__ __forceinline__ float bf_hi(unsigned w) { return __uint_as_float(w & 0xffff0000u); }
;     __device__ __forceinline__ void operator()(f32x4 (&acc)[2][2][4][2], const Unit& u, int wr, int wc, int fr, int fq) const {
;     ...
;                     if (u.tag == 0) {
;                         const u32x4 gn = *(const u32x4*)(GNA + ro + bj * 32);
;                         const float en[8] = {bf_lo(gn.x), bf_hi(gn.x), bf_lo(gn.y), bf_hi(gn.y), bf_lo(gn.z), bf_hi(gn.z), bf_lo(gn.w), bf_hi(gn.w)};
; #pragma unroll
;                         for (int e = 0; e < 8; ++e) {
;                             const float r = (1.0f + __builtin_amdgcn_exp2f(-1.4426950408889634f * ed[e])) * __builtin_amdgcn_rcpf(1.0f + __builtin_amdgcn_exp2f(-1.4426950408889634f * en[e]));
;                             acc[ai][bj][m][e >> 2][e & 3] *= r; }
.LBB0_637:
	global_load_dwordx4 v[182:185], v[6:7], off offset:64 nt
	v_pk_add_f32 v[6:7], v[160:161], 1.0 op_sel_hi:[1,0]
	v_pk_add_f32 v[158:159], v[158:159], 1.0 op_sel_hi:[1,0]
	v_pk_add_f32 v[156:157], v[156:157], 1.0 op_sel_hi:[1,0]
	v_pk_add_f32 v[8:9], v[8:9], 1.0 op_sel_hi:[1,0]
	s_waitcnt vmcnt(0)
	v_lshlrev_b32_e32 v5, 16, v182
	v_and_b32_e32 v160, 0xffff0000, v182
	v_lshlrev_b32_e32 v161, 16, v183
	v_and_b32_e32 v162, 0xffff0000, v183
	v_lshlrev_b32_e32 v163, 16, v184
	v_and_b32_e32 v181, 0xffff0000, v184
	v_lshlrev_b32_e32 v182, 16, v185
	v_and_b32_e32 v183, 0xffff0000, v185
	v_mul_f32_e32 v5, 0xbfb8aa3b, v5
	v_mul_f32_e32 v160, 0xbfb8aa3b, v160
	v_mul_f32_e32 v161, 0xbfb8aa3b, v161
	v_mul_f32_e32 v162, 0xbfb8aa3b, v162
	v_mul_f32_e32 v163, 0xbfb8aa3b, v163
	v_mul_f32_e32 v181, 0xbfb8aa3b, v181
	v_mul_f32_e32 v182, 0xbfb8aa3b, v182
	v_mul_f32_e32 v183, 0xbfb8aa3b, v183
	v_exp_f32_e32 v5, v5
	v_exp_f32_e32 v160, v160
	v_exp_f32_e32 v161, v161
	v_exp_f32_e32 v162, v162
	v_exp_f32_e32 v163, v163
	v_exp_f32_e32 v181, v181
	v_exp_f32_e32 v182, v182
	v_exp_f32_e32 v183, v183
	v_add_f32_e32 v5, 1.0, v5
	v_add_f32_e32 v184, 1.0, v160
	v_add_f32_e32 v185, 1.0, v161
	v_add_f32_e32 v186, 1.0, v162
	v_add_f32_e32 v187, 1.0, v163
	v_add_f32_e32 v181, 1.0, v181
	v_add_f32_e32 v188, 1.0, v182
	v_add_f32_e32 v189, 1.0, v183
	v_rcp_f32_e32 v160, v5
	v_rcp_f32_e32 v161, v184
	v_rcp_f32_e32 v162, v185
	v_rcp_f32_e32 v163, v186
	v_rcp_f32_e32 v182, v187
	v_rcp_f32_e32 v183, v181
	v_rcp_f32_e32 v184, v188
	v_rcp_f32_e32 v185, v189
	v_pk_mul_f32 v[158:159], v[158:159], v[160:161]
	v_pk_mul_f32 v[6:7], v[6:7], v[162:163]
	v_pk_mul_f32 v[8:9], v[8:9], v[182:183]
	v_pk_mul_f32 v[156:157], v[156:157], v[184:185]
	v_pk_mul_f32 v[24:25], v[24:25], v[6:7]
	v_pk_mul_f32 v[22:23], v[22:23], v[158:159]
	v_pk_mul_f32 v[20:21], v[20:21], v[156:157]
	v_pk_mul_f32 v[18:19], v[18:19], v[8:9]
	s_and_b64 vcc, exec, s[4:5]
	s_cbranch_vccz .LBB0_616
	s_branch .LBB0_617

; __device__ __forceinline__ float bf_lo(unsigned w) { return __uint_as_float(w << 16); }
; __device__ __forceinline__ float bf_hi(unsigned w) { return __uint_as_float(w & 0xffff0000u); }
;     __device__ __forceinline__ void operator()(f32x4 (&acc)[2][2][4][2], const Unit& u, int wr, int wc, int fr, int fq) const {
;     ...
;                     if (u.tag == 0) {
;                         const u32x4 gn = *(const u32x4*)(GNA + ro + bj * 32);
;                         const float en[8] = {bf_lo(gn.x), bf_hi(gn.x), bf_lo(gn.y), bf_hi(gn.y), bf_lo(gn.z), bf_hi(gn.z), bf_lo(gn.w), bf_hi(gn.w)};
; #pragma unroll
;                         for (int e = 0; e < 8; ++e) {
;                             const float r = (1.0f + __builtin_amdgcn_exp2f(-1.4426950408889634f * ed[e])) * __builtin_amdgcn_rcpf(1.0f + __builtin_amdgcn_exp2f(-1.4426950408889634f * en[e]));
;                             acc[ai][bj][m][e >> 2][e & 3] *= r; }
.LBB0_639:
	global_load_dwordx4 v[158:161], v[2:3], off offset:64 nt
	v_pk_add_f32 v[2:3], v[156:157], 1.0 op_sel_hi:[1,0]
	v_pk_add_f32 v[8:9], v[8:9], 1.0 op_sel_hi:[1,0]
	v_pk_add_f32 v[6:7], v[6:7], 1.0 op_sel_hi:[1,0]
	v_pk_add_f32 v[4:5], v[4:5], 1.0 op_sel_hi:[1,0]
	s_waitcnt vmcnt(0)
	v_lshlrev_b32_e32 v156, 16, v158
	v_and_b32_e32 v157, 0xffff0000, v158
	v_lshlrev_b32_e32 v158, 16, v159
	v_and_b32_e32 v159, 0xffff0000, v159
	v_lshlrev_b32_e32 v162, 16, v160
	v_and_b32_e32 v160, 0xffff0000, v160
	v_lshlrev_b32_e32 v163, 16, v161
	v_and_b32_e32 v161, 0xffff0000, v161
	v_mul_f32_e32 v156, 0xbfb8aa3b, v156
	v_mul_f32_e32 v157, 0xbfb8aa3b, v157
	v_mul_f32_e32 v158, 0xbfb8aa3b, v158
	v_mul_f32_e32 v159, 0xbfb8aa3b, v159
	v_mul_f32_e32 v162, 0xbfb8aa3b, v162
	v_mul_f32_e32 v160, 0xbfb8aa3b, v160
	v_mul_f32_e32 v163, 0xbfb8aa3b, v163
	v_mul_f32_e32 v161, 0xbfb8aa3b, v161
	v_exp_f32_e32 v156, v156
	v_exp_f32_e32 v157, v157
	v_exp_f32_e32 v158, v158
	v_exp_f32_e32 v159, v159
	v_exp_f32_e32 v162, v162
	v_exp_f32_e32 v160, v160
	v_exp_f32_e32 v163, v163
	v_exp_f32_e32 v161, v161
	v_add_f32_e32 v156, 1.0, v156
	v_add_f32_e32 v157, 1.0, v157
	v_add_f32_e32 v158, 1.0, v158
	v_add_f32_e32 v159, 1.0, v159
	v_add_f32_e32 v162, 1.0, v162
	v_add_f32_e32 v181, 1.0, v160
	v_add_f32_e32 v163, 1.0, v163
	v_add_f32_e32 v182, 1.0, v161
	v_rcp_f32_e32 v156, v156
	v_rcp_f32_e32 v157, v157
	v_rcp_f32_e32 v158, v158
	v_rcp_f32_e32 v159, v159
	v_rcp_f32_e32 v160, v162
	v_rcp_f32_e32 v161, v181
	v_rcp_f32_e32 v162, v163
	v_rcp_f32_e32 v163, v182
	v_pk_mul_f32 v[8:9], v[8:9], v[156:157]
	v_pk_mul_f32 v[2:3], v[2:3], v[158:159]
	v_pk_mul_f32 v[4:5], v[4:5], v[160:161]
	v_pk_mul_f32 v[6:7], v[6:7], v[162:163]
	v_pk_mul_f32 v[16:17], v[16:17], v[2:3]
	v_pk_mul_f32 v[14:15], v[14:15], v[8:9]
	v_pk_mul_f32 v[12:13], v[12:13], v[6:7]
	v_pk_mul_f32 v[10:11], v[10:11], v[4:5]
	s_mov_b64 s[4:5], -1
	s_and_b64 vcc, exec, s[50:51]
	s_cbranch_vccz .LBB0_554
